# ssd chunk-state unit: all 12 channel blocks read conv weights/bias from the LDS copy
# speedup vs baseline: 1.0362x; 1.0133x over previous
; DI void ssd_local_unit(Frame& F, int l, int ch, int g) {
;     ...
;     const float* cw = inp(F, I_CONVW) + (size_t)l * 4 * XC; const float* cb = inp(F, I_CONVB) + (size_t)l * XC;
;     const int s = F.tid >> 2, cg = F.tid & 3;
;     float okm[4]; int spc[4];
; #pragma unroll
;     for (int j = 0; j < 4; ++j) { const int sp = s - 3 + j; const bool ok = cpos * CHUNK + sp >= 0; okm[j] = ok ? 1.f : 0.f; spc[j] = ok ? sp : s; }
;     auto load_part = [&](const int part, v4u (&raw)[4][4]) {
; #pragma unroll
;         for (int cc = 0; cc < 4; ++cc)
; #pragma unroll
;             for (int j = 0; j < 4; ++j) raw[cc][j] = *(const v4u*)(proj + (size_t)(t0 + spc[j]) * PP + O_XBC + part * 256 + g * 128 + cg * 32 + cc * 8); };
;     auto do_part = [&](const int part, const v4u (&raw)[4][4]) {
; #pragma unroll
;         for (int cc = 0; cc < 4; ++cc) {
;             const int lc = cg * 32 + cc * 8, c0 = part * 256 + g * 128 + lc;
;             float acc[8];
;             { const f32x4 b0 = *(const f32x4*)(cb + c0), b1 = *(const f32x4*)(cb + c0 + 4);
; #pragma unroll
;               for (int e = 0; e < 4; ++e) { acc[e] = b0[e]; acc[4 + e] = b1[e]; } }
; #pragma unroll
;             for (int j = 0; j < 4; ++j) { float x[8]; unpack8(raw[cc][j], x);
;                 const f32x4 w0 = *(const f32x4*)(cw + j * XC + c0), w1 = *(const f32x4*)(cw + j * XC + c0 + 4);
; #pragma unroll
;                 for (int e = 0; e < 4; ++e) { acc[e] += w0[e] * okm[j] * x[e]; acc[4 + e] += w1[e] * okm[j] * x[4 + e]; } }
; #pragma unroll
;             for (int e = 0; e < 8; ++e) acc[e] = silu_f(acc[e]);
;             v4u o; o.x = pk2h(acc[0], acc[1]); o.y = pk2h(acc[2], acc[3]); o.z = pk2h(acc[4], acc[5]); o.w = pk2h(acc[6], acc[7]);
;             *(v4u*)(xbcc + (size_t)(t0 + s) * XC + c0) = o;
;             if (part == 0) { const int r2 = lc >> 6; const float dtv = DT[r2 * 128 + s], sc = dtv * __expf(AC[r2 * 128 + 127] - AC[r2 * 128 + s]);
; #pragma unroll
;                 for (int e = 0; e < 8; ++e) { XWT[(lc + e) * LP + s] = (bf16)f2bf(acc[e] * sc); XD[(lc + e) * LP + s] = (bf16)f2bf(acc[e] * dtv); } }
;             else if (part == 1) {
; #pragma unroll
;                 for (int e = 0; e < 8; ++e) BT[(lc + e) * LP + s] = (bf16)f2bf(acc[e]); }
;         } };
;     v4u ra[4][4], rb[4][4];
;     load_part(1, ra);
;     ssd_vectors(F, l, t0, g, DT, AC, RED);
;     load_part(2, rb);
.LBB0_838:
	v_cndmask_b32_e64 v136, 0, 1.0, s[4:5]
	s_add_i32 s4, s19, 0x11000
	s_mul_i32 s0, s28, 0x3000
	s_add_u32 s0, s45, s0
	s_mul_hi_i32 s1, s28, 0x3000
	v_cndmask_b32_e64 v138, 0, 1.0, s[2:3]
	s_addc_u32 s1, s43, s1
	s_mul_i32 s2, s28, 0xc00
	s_add_u32 s2, s42, s2
	s_mul_hi_i32 s3, s28, 0xc00
	v_lshlrev_b32_e32 v141, 5, v137
	s_addc_u32 s3, s44, s3
	s_lshl_b32 s52, s40, 1
	v_lshl_add_u64 v[52:53], v[52:53], 0, s[52:53]
	v_lshlrev_b32_e32 v66, 1, v141
	v_mov_b32_e32 v67, v3
	v_cndmask_b32_e64 v140, 0, 1.0, vcc
	v_cmp_lt_i32_e32 vcc, s30, v1
	v_lshl_add_u64 v[52:53], v[52:53], 0, v[66:67]
	v_lshl_add_u64 v[58:59], v[52:53], 0, s[84:85]
	v_cndmask_b32_e64 v134, 0, 1.0, vcc
	v_add_co_u32_e32 v52, vcc, s64, v52
	v_lshl_add_u64 v[56:57], v[56:57], 0, s[52:53]
	s_nop 0
	v_addc_co_u32_e32 v53, vcc, 0, v53, vcc
	v_lshl_add_u64 v[56:57], v[56:57], 0, v[66:67]
	v_lshl_add_u64 v[62:63], v[56:57], 0, s[84:85]
	v_add_co_u32_e32 v56, vcc, s64, v56
	v_lshl_add_u64 v[60:61], v[60:61], 0, s[52:53]
	s_nop 0
	v_addc_co_u32_e32 v57, vcc, 0, v57, vcc
	v_lshl_add_u64 v[60:61], v[60:61], 0, v[66:67]
	v_lshl_add_u64 v[80:81], v[60:61], 0, s[84:85]
	v_add_co_u32_e32 v60, vcc, s64, v60
	v_lshl_add_u64 v[64:65], v[64:65], 0, s[52:53]
	s_nop 0
	v_addc_co_u32_e32 v61, vcc, 0, v61, vcc
	v_lshl_add_u64 v[64:65], v[64:65], 0, v[66:67]
	v_or_b32_e32 v152, s40, v141
	v_mov_b32_e32 v153, v3
	v_lshl_add_u64 v[96:97], v[64:65], 0, s[84:85]
	v_add_co_u32_e32 v64, vcc, s64, v64
	v_lshlrev_b64 v[142:143], 2, v[152:153]
	s_nop 0
	v_addc_co_u32_e32 v65, vcc, 0, v65, vcc
	v_lshl_add_u64 v[144:145], s[0:1], 0, v[142:143]
	v_lshl_add_u64 v[146:147], s[2:3], 0, v[142:143]
	s_mov_b64 s[6:7], 0x400
	v_add_co_u32_e32 v148, vcc, s64, v144
	s_mov_b64 s[94:95], vcc
	v_cmp_gt_u32_e32 vcc, 0x1e0, v132
	s_and_saveexec_b64 s[92:93], vcc
	v_lshrrev_b32_e32 v202, 5, v132
	v_and_b32_e32 v203, 31, v132
	v_mul_u32_u24_e32 v204, 11, v202
	v_lshrrev_b32_e32 v204, 5, v204
	v_mul_u32_u24_e32 v205, 3, v204
	v_sub_u32_e32 v205, v202, v205
	v_mul_u32_u24_e32 v206, 0xc00, v204
	v_cmp_eq_u32_e32 vcc, 4, v204
	s_nop 1
	v_cndmask_b32_e32 v206, v206, v3, vcc
	v_lshl_add_u32 v206, v205, 10, v206
	v_lshl_add_u32 v206, v203, 4, v206
	s_lshl_b32 s72, s40, 2
	v_add_u32_e32 v206, s72, v206
	v_mov_b32_e32 v208, s0
	v_mov_b32_e32 v207, s2
	v_cndmask_b32_e32 v208, v208, v207, vcc
	v_mov_b32_e32 v209, s1
	v_mov_b32_e32 v207, s3
	v_cndmask_b32_e32 v209, v209, v207, vcc
	v_add_co_u32_e32 v208, vcc, v208, v206
	s_nop 1
	v_addc_co_u32_e32 v209, vcc, 0, v209, vcc
	global_load_dwordx4 v[210:213], v[208:209], off
	v_lshl_add_u32 v214, v132, 4, s19
	v_add_u32_e32 v214, 0x1b000, v214
	s_waitcnt vmcnt(0)
	ds_write_b128 v214, v[210:213]
	s_or_b64 exec, exec, s[92:93]
	v_lshl_add_u32 v215, v137, 7, s19
	v_add_u32_e32 v215, 0x1b000, v215
	s_mov_b64 vcc, s[94:95]
	s_waitcnt lgkmcnt(0)
	s_barrier
	global_load_dwordx4 v[100:103], v[52:53], off
	s_nop 0
	global_load_dwordx4 v[52:55], v[58:59], off offset:48
	global_load_dwordx4 v[68:71], v[58:59], off offset:32
	global_load_dwordx4 v[84:87], v[58:59], off offset:16
	global_load_dwordx4 v[104:107], v[56:57], off
	s_nop 0
	global_load_dwordx4 v[56:59], v[62:63], off offset:48
	global_load_dwordx4 v[72:75], v[62:63], off offset:32
	global_load_dwordx4 v[88:91], v[62:63], off offset:16
	global_load_dwordx4 v[108:111], v[60:61], off
	s_nop 0
	global_load_dwordx4 v[60:63], v[80:81], off offset:48
	global_load_dwordx4 v[76:79], v[80:81], off offset:32
	global_load_dwordx4 v[92:95], v[80:81], off offset:16
	global_load_dwordx4 v[112:115], v[64:65], off
	s_nop 0
	global_load_dwordx4 v[64:67], v[96:97], off offset:48
	global_load_dwordx4 v[80:83], v[96:97], off offset:32
	s_nop 0
	global_load_dwordx4 v[96:99], v[96:97], off offset:16
	s_nop 0
	ds_read_b128 v[162:165], v215 offset:6672
	ds_read_b128 v[166:169], v215 offset:6656
	v_lshl_add_u64 v[142:143], v[144:145], 0, s[6:7]
	ds_read_b128 v[170:173], v215 offset:528
	ds_read_b128 v[174:177], v215 offset:512
	ds_read_b128 v[178:181], v215 offset:2064
	ds_read_b128 v[182:185], v215 offset:2048
	v_addc_co_u32_e32 v149, vcc, 0, v145, vcc
	s_movk_i32 s42, 0x2000
	s_mov_b64 s[6:7], 0x1c00
	v_add_co_u32_e32 v150, vcc, s42, v144
	v_lshl_add_u64 v[142:143], v[144:145], 0, s[6:7]
	ds_read_b128 v[186:189], v215 offset:3584
	ds_read_b128 v[190:193], v215 offset:3600
	s_mov_b64 s[6:7], 0x2800
	v_addc_co_u32_e32 v151, vcc, 0, v145, vcc
	v_lshl_add_u64 v[142:143], v[144:145], 0, s[6:7]
	ds_read_b128 v[194:197], v215 offset:5120
	ds_read_b128 v[198:201], v215 offset:5136
	s_waitcnt vmcnt(16) lgkmcnt(0)
; __device__ __forceinline__ unsigned f2bf(float f) { unsigned u = __builtin_bit_cast(unsigned, f); return (u + 0x7fffu + ((u >> 16) & 1u)) >> 16; }
; DI unsigned pk2h(float lo, float hi) { const f32x2h_t v = {lo, hi}; return __builtin_bit_cast(unsigned, __builtin_convertvector(v, bf16x2h_t)); }
; DI float silu_f(float x) { return x * __builtin_amdgcn_rcpf(1.f + __expf(-x)); }
; DI void ssd_local_unit(Frame& F, int l, int ch, int g) {
;     ...
;     auto do_part = [&](const int part, const v4u (&raw)[4][4]) {
; #pragma unroll
;         for (int cc = 0; cc < 4; ++cc) {
;             const int lc = cg * 32 + cc * 8, c0 = part * 256 + g * 128 + lc;
;             float acc[8];
;             { const f32x4 b0 = *(const f32x4*)(cb + c0), b1 = *(const f32x4*)(cb + c0 + 4);
; #pragma unroll
;               for (int e = 0; e < 4; ++e) { acc[e] = b0[e]; acc[4 + e] = b1[e]; } }
; #pragma unroll
;             for (int j = 0; j < 4; ++j) { float x[8]; unpack8(raw[cc][j], x);
;                 const f32x4 w0 = *(const f32x4*)(cw + j * XC + c0), w1 = *(const f32x4*)(cw + j * XC + c0 + 4);
; #pragma unroll
;                 for (int e = 0; e < 4; ++e) { acc[e] += w0[e] * okm[j] * x[e]; acc[4 + e] += w1[e] * okm[j] * x[4 + e]; } }
; #pragma unroll
;             for (int e = 0; e < 8; ++e) acc[e] = silu_f(acc[e]);
;             v4u o; o.x = pk2h(acc[0], acc[1]); o.y = pk2h(acc[2], acc[3]); o.z = pk2h(acc[4], acc[5]); o.w = pk2h(acc[6], acc[7]);
;             *(v4u*)(xbcc + (size_t)(t0 + s) * XC + c0) = o;
;             if (part == 0) { const int r2 = lc >> 6; const float dtv = DT[r2 * 128 + s], sc = dtv * __expf(AC[r2 * 128 + 127] - AC[r2 * 128 + s]);
; #pragma unroll
;                 for (int e = 0; e < 8; ++e) { XWT[(lc + e) * LP + s] = (bf16)f2bf(acc[e] * sc); XD[(lc + e) * LP + s] = (bf16)f2bf(acc[e] * dtv); } }
;             else if (part == 1) {
; #pragma unroll
;                 for (int e = 0; e < 8; ++e) BT[(lc + e) * LP + s] = (bf16)f2bf(acc[e]); }
	v_lshlrev_b32_e32 v142, 16, v116
	v_and_b32_e32 v143, 0xffff0000, v116
	v_lshlrev_b32_e32 v116, 16, v117
	v_and_b32_e32 v117, 0xffff0000, v117
	s_movk_i32 s5, 0x2200
	s_nop 0
	v_pk_mul_f32 v[174:175], v[140:141], v[174:175] op_sel_hi:[0,1]
	v_pk_fma_f32 v[142:143], v[174:175], v[142:143], v[166:167]
	v_lshlrev_b32_e32 v166, 16, v120
	v_and_b32_e32 v167, 0xffff0000, v120
	s_nop 0
	v_pk_mul_f32 v[174:175], v[138:139], v[182:183] op_sel_hi:[0,1]
	v_pk_fma_f32 v[142:143], v[174:175], v[166:167], v[142:143]
	v_lshlrev_b32_e32 v166, 16, v124
	v_and_b32_e32 v167, 0xffff0000, v124
	v_lshlrev_b32_e32 v120, 16, v121
	s_nop 0
	v_pk_mul_f32 v[174:175], v[136:137], v[186:187] op_sel_hi:[0,1]
	v_pk_fma_f32 v[142:143], v[174:175], v[166:167], v[142:143]
	v_lshlrev_b32_e32 v166, 16, v128
	v_and_b32_e32 v167, 0xffff0000, v128
	v_and_b32_e32 v121, 0xffff0000, v121
	s_nop 0
	v_pk_mul_f32 v[174:175], v[134:135], v[194:195] op_sel_hi:[0,1]
	v_pk_fma_f32 v[142:143], v[174:175], v[166:167], v[142:143]
	s_nop 0
	v_mul_f32_e32 v0, 0xbfb8aa3b, v142
	v_exp_f32_e32 v0, v0
	s_nop 0
	v_add_f32_e32 v0, 1.0, v0
	v_rcp_f32_e32 v166, v0
	v_mul_f32_e32 v0, 0xbfb8aa3b, v143
	v_exp_f32_e32 v0, v0
	s_nop 0
	v_add_f32_e32 v0, 1.0, v0
	v_rcp_f32_e32 v167, v0
	s_nop 0
	v_pk_mul_f32 v[166:167], v[142:143], v[166:167]
	v_pk_mul_f32 v[142:143], v[140:141], v[176:177] op_sel_hi:[0,1]
	v_pk_fma_f32 v[116:117], v[142:143], v[116:117], v[168:169]
	v_pk_mul_f32 v[142:143], v[138:139], v[184:185] op_sel_hi:[0,1]
	v_pk_fma_f32 v[116:117], v[142:143], v[120:121], v[116:117]
	v_lshlrev_b32_e32 v120, 16, v125
	v_and_b32_e32 v121, 0xffff0000, v125
	v_pk_mul_f32 v[124:125], v[136:137], v[188:189] op_sel_hi:[0,1]
	v_pk_fma_f32 v[116:117], v[124:125], v[120:121], v[116:117]
	v_lshlrev_b32_e32 v120, 16, v129
	v_and_b32_e32 v121, 0xffff0000, v129
	v_pk_mul_f32 v[124:125], v[134:135], v[196:197] op_sel_hi:[0,1]
	v_pk_fma_f32 v[116:117], v[124:125], v[120:121], v[116:117]
	v_pk_mul_f32 v[124:125], v[140:141], v[170:171] op_sel_hi:[0,1]
	v_mul_f32_e32 v0, 0xbfb8aa3b, v116
	v_exp_f32_e32 v0, v0
	v_pk_mul_f32 v[128:129], v[138:139], v[178:179] op_sel_hi:[0,1]
	v_add_f32_e32 v0, 1.0, v0
	v_rcp_f32_e32 v120, v0
	v_mul_f32_e32 v0, 0xbfb8aa3b, v117
	v_exp_f32_e32 v0, v0
	s_nop 0
	v_add_f32_e32 v0, 1.0, v0
	v_rcp_f32_e32 v121, v0
	s_nop 0
	v_pk_mul_f32 v[120:121], v[116:117], v[120:121]
	v_lshlrev_b32_e32 v116, 16, v118
	v_and_b32_e32 v117, 0xffff0000, v118
	v_pk_fma_f32 v[116:117], v[124:125], v[116:117], v[162:163]
	v_lshlrev_b32_e32 v124, 16, v122
	v_and_b32_e32 v125, 0xffff0000, v122
	v_pk_fma_f32 v[116:117], v[128:129], v[124:125], v[116:117]
	v_lshlrev_b32_e32 v124, 16, v126
	v_and_b32_e32 v125, 0xffff0000, v126
	v_pk_mul_f32 v[128:129], v[136:137], v[190:191] op_sel_hi:[0,1]
	v_pk_fma_f32 v[116:117], v[128:129], v[124:125], v[116:117]
	v_lshlrev_b32_e32 v124, 16, v130
	v_and_b32_e32 v125, 0xffff0000, v130
	s_waitcnt vmcnt(0)
	v_pk_mul_f32 v[128:129], v[134:135], v[198:199] op_sel_hi:[0,1]
	v_pk_fma_f32 v[116:117], v[128:129], v[124:125], v[116:117]
	v_or_b32_e32 v163, 8, v141
	v_mul_f32_e32 v0, 0xbfb8aa3b, v116
	v_exp_f32_e32 v0, v0
	v_or_b32_e32 v162, 16, v141
	v_lshlrev_b32_e32 v198, 16, v100
	v_and_b32_e32 v199, 0xffff0000, v100
	v_add_f32_e32 v0, 1.0, v0
	v_rcp_f32_e32 v124, v0
	v_mul_f32_e32 v0, 0xbfb8aa3b, v117
	v_exp_f32_e32 v0, v0
	v_lshlrev_b32_e32 v100, 16, v101
	v_and_b32_e32 v101, 0xffff0000, v101
	v_add_f32_e32 v0, 1.0, v0
	v_rcp_f32_e32 v125, v0
	s_nop 0
	v_pk_mul_f32 v[124:125], v[116:117], v[124:125]
	v_lshlrev_b32_e32 v116, 16, v119
	v_and_b32_e32 v117, 0xffff0000, v119
	v_pk_mul_f32 v[118:119], v[140:141], v[172:173] op_sel_hi:[0,1]
	v_pk_fma_f32 v[116:117], v[118:119], v[116:117], v[164:165]
	v_lshlrev_b32_e32 v118, 16, v123
	v_and_b32_e32 v119, 0xffff0000, v123
	v_pk_mul_f32 v[122:123], v[138:139], v[180:181] op_sel_hi:[0,1]
	v_pk_fma_f32 v[116:117], v[122:123], v[118:119], v[116:117]
	v_lshlrev_b32_e32 v118, 16, v127
	v_and_b32_e32 v119, 0xffff0000, v127
	v_pk_mul_f32 v[122:123], v[136:137], v[192:193] op_sel_hi:[0,1]
	v_pk_fma_f32 v[116:117], v[122:123], v[118:119], v[116:117]
	v_lshlrev_b32_e32 v118, 16, v131
	v_and_b32_e32 v119, 0xffff0000, v131
	v_pk_mul_f32 v[122:123], v[134:135], v[200:201] op_sel_hi:[0,1]
	v_pk_fma_f32 v[116:117], v[122:123], v[118:119], v[116:117]
	v_mov_b64_e32 v[126:127], s[20:21]
	v_mul_f32_e32 v0, 0xbfb8aa3b, v116
	v_exp_f32_e32 v0, v0
	v_mad_i64_i32 v[126:127], s[6:7], v135, s65, v[126:127]
	s_mov_b64 s[6:7], 0x1c100000
	v_add_f32_e32 v0, 1.0, v0
	v_rcp_f32_e32 v118, v0
	v_mul_f32_e32 v0, 0xbfb8aa3b, v117
	v_exp_f32_e32 v0, v0
	v_lshl_add_u64 v[142:143], v[126:127], 0, s[6:7]
	v_lshlrev_b32_e32 v126, 1, v152
	v_mov_b32_e32 v127, v3
	v_add_f32_e32 v0, 1.0, v0
	v_rcp_f32_e32 v119, v0
	v_lshlrev_b32_e32 v164, 1, v1
	v_lshl_add_u64 v[152:153], v[142:143], 0, v[126:127]
	v_add_u32_e32 v135, s19, v164
	v_pk_mul_f32 v[122:123], v[116:117], v[118:119]
	v_cvt_pk_bf16_f32 v116, v166, v167
	v_cvt_pk_bf16_f32 v117, v120, v121
	v_cvt_pk_bf16_f32 v118, v124, v125
	v_cvt_pk_bf16_f32 v119, v122, v123
	v_bfe_u32 v0, v166, 16, 1
	global_store_dwordx4 v[152:153], v[116:119], off offset:512
	v_add3_u32 v0, v166, v0, s97
	s_mov_b64 s[6:7], 0x420
	v_mad_u32_u24 v116, v137, s5, v135
	ds_write_b16_d16_hi v116, v0 offset:34816
	v_bfe_u32 v0, v167, 16, 1
	v_add3_u32 v0, v167, v0, s97
	ds_write_b16_d16_hi v116, v0 offset:35088
	v_bfe_u32 v0, v120, 16, 1
	v_add3_u32 v0, v120, v0, s97
	ds_write_b16_d16_hi v116, v0 offset:35360
	v_bfe_u32 v0, v121, 16, 1
	v_add3_u32 v0, v121, v0, s97
	ds_write_b16_d16_hi v116, v0 offset:35632
	v_bfe_u32 v0, v124, 16, 1
	v_add3_u32 v0, v124, v0, s97
	ds_write_b16_d16_hi v116, v0 offset:35904
	v_bfe_u32 v0, v125, 16, 1
	v_add3_u32 v0, v125, v0, s97
	ds_write_b16_d16_hi v116, v0 offset:36176
	v_bfe_u32 v0, v122, 16, 1
	v_add3_u32 v0, v122, v0, s97
	ds_write_b16_d16_hi v116, v0 offset:36448
	v_bfe_u32 v0, v123, 16, 1
	v_add3_u32 v0, v123, v0, s97
	ds_write_b16_d16_hi v116, v0 offset:36720
	ds_read_b128 v[118:121], v215 offset:6704
	ds_read_b128 v[122:125], v215 offset:6688
	v_lshl_add_u64 v[130:131], v[144:145], 0, s[6:7]
	ds_read_b128 v[126:129], v215 offset:560
	ds_read_b128 v[166:169], v215 offset:544
	ds_read_b128 v[170:173], v215 offset:2096
	ds_read_b128 v[174:177], v215 offset:2080
	s_mov_b64 s[6:7], 0x1c20
	v_lshl_add_u64 v[130:131], v[144:145], 0, s[6:7]
	ds_read_b128 v[178:181], v215 offset:3616
	ds_read_b128 v[182:185], v215 offset:3632
	s_mov_b64 s[6:7], 0x2820
	v_lshl_add_u64 v[130:131], v[144:145], 0, s[6:7]
	ds_read_b128 v[186:189], v215 offset:5152
	ds_read_b128 v[190:193], v215 offset:5168
	v_lshlrev_b32_e32 v130, 16, v36
	v_and_b32_e32 v131, 0xffff0000, v36
	v_lshlrev_b32_e32 v36, 16, v37
	v_and_b32_e32 v37, 0xffff0000, v37
	s_mov_b64 s[6:7], 0x440
	s_waitcnt lgkmcnt(0)
; __device__ __forceinline__ unsigned f2bf(float f) { unsigned u = __builtin_bit_cast(unsigned, f); return (u + 0x7fffu + ((u >> 16) & 1u)) >> 16; }
; DI unsigned pk2h(float lo, float hi) { const f32x2h_t v = {lo, hi}; return __builtin_bit_cast(unsigned, __builtin_convertvector(v, bf16x2h_t)); }
; DI float silu_f(float x) { return x * __builtin_amdgcn_rcpf(1.f + __expf(-x)); }
; DI void ssd_local_unit(Frame& F, int l, int ch, int g) {
;     ...
;     auto do_part = [&](const int part, const v4u (&raw)[4][4]) {
; #pragma unroll
;         for (int cc = 0; cc < 4; ++cc) {
;             const int lc = cg * 32 + cc * 8, c0 = part * 256 + g * 128 + lc;
;             float acc[8];
;             { const f32x4 b0 = *(const f32x4*)(cb + c0), b1 = *(const f32x4*)(cb + c0 + 4);
; #pragma unroll
;               for (int e = 0; e < 4; ++e) { acc[e] = b0[e]; acc[4 + e] = b1[e]; } }
; #pragma unroll
;             for (int j = 0; j < 4; ++j) { float x[8]; unpack8(raw[cc][j], x);
;                 const f32x4 w0 = *(const f32x4*)(cw + j * XC + c0), w1 = *(const f32x4*)(cw + j * XC + c0 + 4);
; #pragma unroll
;                 for (int e = 0; e < 4; ++e) { acc[e] += w0[e] * okm[j] * x[e]; acc[4 + e] += w1[e] * okm[j] * x[4 + e]; } }
; #pragma unroll
;             for (int e = 0; e < 8; ++e) acc[e] = silu_f(acc[e]);
;             v4u o; o.x = pk2h(acc[0], acc[1]); o.y = pk2h(acc[2], acc[3]); o.z = pk2h(acc[4], acc[5]); o.w = pk2h(acc[6], acc[7]);
;             *(v4u*)(xbcc + (size_t)(t0 + s) * XC + c0) = o;
;             if (part == 0) { const int r2 = lc >> 6; const float dtv = DT[r2 * 128 + s], sc = dtv * __expf(AC[r2 * 128 + 127] - AC[r2 * 128 + s]);
; #pragma unroll
;                 for (int e = 0; e < 8; ++e) { XWT[(lc + e) * LP + s] = (bf16)f2bf(acc[e] * sc); XD[(lc + e) * LP + s] = (bf16)f2bf(acc[e] * dtv); } }
;             else if (part == 1) {
; #pragma unroll
;                 for (int e = 0; e < 8; ++e) BT[(lc + e) * LP + s] = (bf16)f2bf(acc[e]); }
	v_pk_mul_f32 v[166:167], v[140:141], v[166:167] op_sel_hi:[0,1]
	v_pk_fma_f32 v[122:123], v[166:167], v[130:131], v[122:123]
	v_lshlrev_b32_e32 v130, 16, v40
	v_and_b32_e32 v131, 0xffff0000, v40
	s_nop 0
	v_pk_mul_f32 v[166:167], v[138:139], v[174:175] op_sel_hi:[0,1]
	v_pk_fma_f32 v[122:123], v[166:167], v[130:131], v[122:123]
	v_lshlrev_b32_e32 v130, 16, v44
	v_and_b32_e32 v131, 0xffff0000, v44
	s_nop 0
	v_pk_mul_f32 v[166:167], v[136:137], v[178:179] op_sel_hi:[0,1]
	v_pk_fma_f32 v[122:123], v[166:167], v[130:131], v[122:123]
	v_lshlrev_b32_e32 v130, 16, v48
	v_and_b32_e32 v131, 0xffff0000, v48
	s_nop 0
	v_pk_mul_f32 v[166:167], v[134:135], v[186:187] op_sel_hi:[0,1]
	v_pk_fma_f32 v[122:123], v[166:167], v[130:131], v[122:123]
	v_lshlrev_b32_e32 v40, 16, v41
	v_mul_f32_e32 v0, 0xbfb8aa3b, v122
	v_exp_f32_e32 v0, v0
	v_and_b32_e32 v41, 0xffff0000, v41
	v_add_f32_e32 v0, 1.0, v0
	v_rcp_f32_e32 v130, v0
	v_mul_f32_e32 v0, 0xbfb8aa3b, v123
	v_exp_f32_e32 v0, v0
	s_nop 0
	v_add_f32_e32 v0, 1.0, v0
	v_rcp_f32_e32 v131, v0
	s_nop 0
	v_pk_mul_f32 v[122:123], v[122:123], v[130:131]
	v_pk_mul_f32 v[130:131], v[140:141], v[168:169] op_sel_hi:[0,1]
	v_pk_fma_f32 v[36:37], v[130:131], v[36:37], v[124:125]
	v_pk_mul_f32 v[124:125], v[138:139], v[176:177] op_sel_hi:[0,1]
	v_pk_fma_f32 v[36:37], v[124:125], v[40:41], v[36:37]
	v_lshlrev_b32_e32 v40, 16, v45
	v_and_b32_e32 v41, 0xffff0000, v45
	v_pk_mul_f32 v[44:45], v[136:137], v[180:181] op_sel_hi:[0,1]
	v_pk_fma_f32 v[36:37], v[44:45], v[40:41], v[36:37]
	v_lshlrev_b32_e32 v40, 16, v49
	v_and_b32_e32 v41, 0xffff0000, v49
	v_pk_mul_f32 v[44:45], v[134:135], v[188:189] op_sel_hi:[0,1]
	v_pk_fma_f32 v[36:37], v[44:45], v[40:41], v[36:37]
	v_pk_mul_f32 v[44:45], v[140:141], v[126:127] op_sel_hi:[0,1]
	v_mul_f32_e32 v0, 0xbfb8aa3b, v36
	v_exp_f32_e32 v0, v0
	v_pk_mul_f32 v[48:49], v[138:139], v[170:171] op_sel_hi:[0,1]
	v_add_f32_e32 v0, 1.0, v0
	v_rcp_f32_e32 v40, v0
	v_mul_f32_e32 v0, 0xbfb8aa3b, v37
	v_exp_f32_e32 v0, v0
	s_nop 0
	v_add_f32_e32 v0, 1.0, v0
	v_rcp_f32_e32 v41, v0
	s_nop 0
	v_pk_mul_f32 v[40:41], v[36:37], v[40:41]
	v_lshlrev_b32_e32 v36, 16, v38
	v_and_b32_e32 v37, 0xffff0000, v38
	v_pk_fma_f32 v[36:37], v[44:45], v[36:37], v[118:119]
	v_lshlrev_b32_e32 v44, 16, v42
	v_and_b32_e32 v45, 0xffff0000, v42
	v_pk_fma_f32 v[36:37], v[48:49], v[44:45], v[36:37]
	v_lshlrev_b32_e32 v44, 16, v46
	v_and_b32_e32 v45, 0xffff0000, v46
	v_pk_mul_f32 v[48:49], v[136:137], v[182:183] op_sel_hi:[0,1]
	v_pk_fma_f32 v[36:37], v[48:49], v[44:45], v[36:37]
	v_lshlrev_b32_e32 v44, 16, v50
	v_and_b32_e32 v45, 0xffff0000, v50
	s_nop 0
	v_pk_mul_f32 v[48:49], v[134:135], v[190:191] op_sel_hi:[0,1]
	v_pk_fma_f32 v[36:37], v[48:49], v[44:45], v[36:37]
	s_nop 0
	v_mul_f32_e32 v0, 0xbfb8aa3b, v36
	v_exp_f32_e32 v0, v0
	s_nop 0
	v_add_f32_e32 v0, 1.0, v0
	v_rcp_f32_e32 v44, v0
	v_mul_f32_e32 v0, 0xbfb8aa3b, v37
	v_exp_f32_e32 v0, v0
	s_nop 0
	v_add_f32_e32 v0, 1.0, v0
	v_rcp_f32_e32 v45, v0
	s_nop 0
	v_pk_mul_f32 v[44:45], v[36:37], v[44:45]
	v_lshlrev_b32_e32 v36, 16, v39
	v_and_b32_e32 v37, 0xffff0000, v39
	v_pk_mul_f32 v[38:39], v[140:141], v[128:129] op_sel_hi:[0,1]
	v_pk_fma_f32 v[36:37], v[38:39], v[36:37], v[120:121]
	v_lshlrev_b32_e32 v38, 16, v43
	v_and_b32_e32 v39, 0xffff0000, v43
	v_pk_mul_f32 v[42:43], v[138:139], v[172:173] op_sel_hi:[0,1]
	v_pk_fma_f32 v[36:37], v[42:43], v[38:39], v[36:37]
	v_lshlrev_b32_e32 v38, 16, v47
	v_and_b32_e32 v39, 0xffff0000, v47
	v_pk_mul_f32 v[42:43], v[136:137], v[184:185] op_sel_hi:[0,1]
	v_pk_fma_f32 v[36:37], v[42:43], v[38:39], v[36:37]
	v_lshlrev_b32_e32 v38, 16, v51
	v_and_b32_e32 v39, 0xffff0000, v51
	v_pk_mul_f32 v[42:43], v[134:135], v[192:193] op_sel_hi:[0,1]
	v_pk_fma_f32 v[36:37], v[42:43], v[38:39], v[36:37]
	s_nop 0
	v_mul_f32_e32 v0, 0xbfb8aa3b, v36
	v_exp_f32_e32 v0, v0
	s_nop 0
	v_add_f32_e32 v0, 1.0, v0
	v_rcp_f32_e32 v38, v0
	v_mul_f32_e32 v0, 0xbfb8aa3b, v37
	v_exp_f32_e32 v0, v0
	s_nop 0
	v_add_f32_e32 v0, 1.0, v0
	v_rcp_f32_e32 v39, v0
	v_bfe_u32 v0, v122, 16, 1
	v_add3_u32 v0, v122, v0, s97
	v_pk_mul_f32 v[42:43], v[36:37], v[38:39]
	v_cvt_pk_bf16_f32 v36, v122, v123
	v_cvt_pk_bf16_f32 v37, v40, v41
	v_cvt_pk_bf16_f32 v38, v44, v45
	v_cvt_pk_bf16_f32 v39, v42, v43
	global_store_dwordx4 v[152:153], v[36:39], off offset:528
	s_nop 1
	v_mad_u32_u24 v36, v163, s66, v135
	ds_write_b16_d16_hi v36, v0 offset:34816
	v_bfe_u32 v0, v123, 16, 1
	v_add3_u32 v0, v123, v0, s97
	ds_write_b16_d16_hi v116, v0 offset:37264
	v_bfe_u32 v0, v40, 16, 1
	v_add3_u32 v0, v40, v0, s97
	ds_write_b16_d16_hi v116, v0 offset:37536
	v_bfe_u32 v0, v41, 16, 1
	v_add3_u32 v0, v41, v0, s97
	ds_write_b16_d16_hi v116, v0 offset:37808
	v_bfe_u32 v0, v44, 16, 1
	v_add3_u32 v0, v44, v0, s97
	ds_write_b16_d16_hi v116, v0 offset:38080
	v_bfe_u32 v0, v45, 16, 1
	v_add3_u32 v0, v45, v0, s97
	ds_write_b16_d16_hi v116, v0 offset:38352
	v_bfe_u32 v0, v42, 16, 1
	v_add3_u32 v0, v42, v0, s97
	ds_write_b16_d16_hi v116, v0 offset:38624
	v_bfe_u32 v0, v43, 16, 1
	v_add3_u32 v0, v43, v0, s97
	ds_write_b16_d16_hi v116, v0 offset:38896
	v_lshl_add_u64 v[122:123], v[144:145], 0, s[6:7]
	ds_read_b128 v[36:39], v215 offset:6736
	ds_read_b128 v[40:43], v215 offset:6720
	ds_read_b128 v[44:47], v215 offset:592
	ds_read_b128 v[48:51], v215 offset:576
	ds_read_b128 v[118:121], v215 offset:2128
	s_nop 0
	ds_read_b128 v[122:125], v215 offset:2112
	s_mov_b64 s[6:7], 0x1c40
	v_lshl_add_u64 v[130:131], v[144:145], 0, s[6:7]
	ds_read_b128 v[126:129], v215 offset:3648
	ds_read_b128 v[166:169], v215 offset:3664
	s_mov_b64 s[6:7], 0x2840
	v_lshl_add_u64 v[130:131], v[144:145], 0, s[6:7]
	ds_read_b128 v[170:173], v215 offset:5184
	ds_read_b128 v[174:177], v215 offset:5200
	v_lshlrev_b32_e32 v130, 16, v20
	v_and_b32_e32 v131, 0xffff0000, v20
	v_lshlrev_b32_e32 v20, 16, v21
	v_and_b32_e32 v21, 0xffff0000, v21
	s_mov_b64 s[6:7], 0x460
	s_waitcnt lgkmcnt(0)
; __device__ __forceinline__ unsigned f2bf(float f) { unsigned u = __builtin_bit_cast(unsigned, f); return (u + 0x7fffu + ((u >> 16) & 1u)) >> 16; }
; DI unsigned pk2h(float lo, float hi) { const f32x2h_t v = {lo, hi}; return __builtin_bit_cast(unsigned, __builtin_convertvector(v, bf16x2h_t)); }
; DI float silu_f(float x) { return x * __builtin_amdgcn_rcpf(1.f + __expf(-x)); }
; DI void ssd_local_unit(Frame& F, int l, int ch, int g) {
;     ...
;     auto do_part = [&](const int part, const v4u (&raw)[4][4]) {
; #pragma unroll
;         for (int cc = 0; cc < 4; ++cc) {
;             const int lc = cg * 32 + cc * 8, c0 = part * 256 + g * 128 + lc;
;             float acc[8];
;             { const f32x4 b0 = *(const f32x4*)(cb + c0), b1 = *(const f32x4*)(cb + c0 + 4);
; #pragma unroll
;               for (int e = 0; e < 4; ++e) { acc[e] = b0[e]; acc[4 + e] = b1[e]; } }
; #pragma unroll
;             for (int j = 0; j < 4; ++j) { float x[8]; unpack8(raw[cc][j], x);
;                 const f32x4 w0 = *(const f32x4*)(cw + j * XC + c0), w1 = *(const f32x4*)(cw + j * XC + c0 + 4);
; #pragma unroll
;                 for (int e = 0; e < 4; ++e) { acc[e] += w0[e] * okm[j] * x[e]; acc[4 + e] += w1[e] * okm[j] * x[4 + e]; } }
; #pragma unroll
;             for (int e = 0; e < 8; ++e) acc[e] = silu_f(acc[e]);
;             v4u o; o.x = pk2h(acc[0], acc[1]); o.y = pk2h(acc[2], acc[3]); o.z = pk2h(acc[4], acc[5]); o.w = pk2h(acc[6], acc[7]);
;             *(v4u*)(xbcc + (size_t)(t0 + s) * XC + c0) = o;
;             if (part == 0) { const int r2 = lc >> 6; const float dtv = DT[r2 * 128 + s], sc = dtv * __expf(AC[r2 * 128 + 127] - AC[r2 * 128 + s]);
; #pragma unroll
;                 for (int e = 0; e < 8; ++e) { XWT[(lc + e) * LP + s] = (bf16)f2bf(acc[e] * sc); XD[(lc + e) * LP + s] = (bf16)f2bf(acc[e] * dtv); } }
;             else if (part == 1) {
; #pragma unroll
;                 for (int e = 0; e < 8; ++e) BT[(lc + e) * LP + s] = (bf16)f2bf(acc[e]); }
	v_pk_mul_f32 v[48:49], v[140:141], v[48:49] op_sel_hi:[0,1]
	v_pk_fma_f32 v[40:41], v[48:49], v[130:131], v[40:41]
	v_lshlrev_b32_e32 v48, 16, v24
	v_and_b32_e32 v49, 0xffff0000, v24
	s_nop 0
	v_pk_mul_f32 v[122:123], v[138:139], v[122:123] op_sel_hi:[0,1]
	v_pk_fma_f32 v[40:41], v[122:123], v[48:49], v[40:41]
	v_lshlrev_b32_e32 v48, 16, v28
	v_and_b32_e32 v49, 0xffff0000, v28
	s_nop 0
	v_pk_mul_f32 v[122:123], v[136:137], v[126:127] op_sel_hi:[0,1]
	v_pk_fma_f32 v[40:41], v[122:123], v[48:49], v[40:41]
	v_lshlrev_b32_e32 v48, 16, v32
	v_and_b32_e32 v49, 0xffff0000, v32
	s_nop 0
	v_pk_mul_f32 v[122:123], v[134:135], v[170:171] op_sel_hi:[0,1]
	v_pk_fma_f32 v[40:41], v[122:123], v[48:49], v[40:41]
	v_lshlrev_b32_e32 v24, 16, v25
	v_mul_f32_e32 v0, 0xbfb8aa3b, v40
	v_exp_f32_e32 v0, v0
	v_and_b32_e32 v25, 0xffff0000, v25
	v_lshlrev_b32_e32 v126, 16, v4
	v_and_b32_e32 v127, 0xffff0000, v4
	v_add_f32_e32 v0, 1.0, v0
	v_rcp_f32_e32 v48, v0
	v_mul_f32_e32 v0, 0xbfb8aa3b, v41
	v_exp_f32_e32 v0, v0
	v_lshlrev_b32_e32 v4, 16, v5
	v_and_b32_e32 v5, 0xffff0000, v5
	v_add_f32_e32 v0, 1.0, v0
	v_rcp_f32_e32 v49, v0
	s_nop 0
	v_pk_mul_f32 v[40:41], v[40:41], v[48:49]
	v_pk_mul_f32 v[48:49], v[140:141], v[50:51] op_sel_hi:[0,1]
	v_pk_fma_f32 v[20:21], v[48:49], v[20:21], v[42:43]
	v_pk_mul_f32 v[42:43], v[138:139], v[124:125] op_sel_hi:[0,1]
	v_pk_fma_f32 v[20:21], v[42:43], v[24:25], v[20:21]
	v_lshlrev_b32_e32 v24, 16, v29
	v_and_b32_e32 v25, 0xffff0000, v29
	v_pk_mul_f32 v[28:29], v[136:137], v[128:129] op_sel_hi:[0,1]
	v_pk_fma_f32 v[20:21], v[28:29], v[24:25], v[20:21]
	v_lshlrev_b32_e32 v24, 16, v33
	v_and_b32_e32 v25, 0xffff0000, v33
	v_pk_mul_f32 v[28:29], v[134:135], v[172:173] op_sel_hi:[0,1]
	v_pk_fma_f32 v[20:21], v[28:29], v[24:25], v[20:21]
	v_pk_mul_f32 v[28:29], v[140:141], v[44:45] op_sel_hi:[0,1]
	v_mul_f32_e32 v0, 0xbfb8aa3b, v20
	v_exp_f32_e32 v0, v0
	v_pk_mul_f32 v[32:33], v[138:139], v[118:119] op_sel_hi:[0,1]
	v_add_f32_e32 v0, 1.0, v0
	v_rcp_f32_e32 v24, v0
	v_mul_f32_e32 v0, 0xbfb8aa3b, v21
	v_exp_f32_e32 v0, v0
	s_nop 0
	v_add_f32_e32 v0, 1.0, v0
	v_rcp_f32_e32 v25, v0
	s_nop 0
	v_pk_mul_f32 v[24:25], v[20:21], v[24:25]
	v_lshlrev_b32_e32 v20, 16, v22
	v_and_b32_e32 v21, 0xffff0000, v22
	v_pk_fma_f32 v[20:21], v[28:29], v[20:21], v[36:37]
	v_lshlrev_b32_e32 v28, 16, v26
	v_and_b32_e32 v29, 0xffff0000, v26
	v_pk_fma_f32 v[20:21], v[32:33], v[28:29], v[20:21]
	v_lshlrev_b32_e32 v28, 16, v30
	v_and_b32_e32 v29, 0xffff0000, v30
	v_pk_mul_f32 v[32:33], v[136:137], v[166:167] op_sel_hi:[0,1]
	v_pk_fma_f32 v[20:21], v[32:33], v[28:29], v[20:21]
	v_lshlrev_b32_e32 v28, 16, v34
	v_and_b32_e32 v29, 0xffff0000, v34
	s_nop 0
	v_pk_mul_f32 v[32:33], v[134:135], v[174:175] op_sel_hi:[0,1]
	v_pk_fma_f32 v[20:21], v[32:33], v[28:29], v[20:21]
	s_nop 0
	v_mul_f32_e32 v0, 0xbfb8aa3b, v20
	v_exp_f32_e32 v0, v0
	s_nop 0
	v_add_f32_e32 v0, 1.0, v0
	v_rcp_f32_e32 v28, v0
	v_mul_f32_e32 v0, 0xbfb8aa3b, v21
	v_exp_f32_e32 v0, v0
	s_nop 0
	v_add_f32_e32 v0, 1.0, v0
	v_rcp_f32_e32 v29, v0
	s_nop 0
	v_pk_mul_f32 v[28:29], v[20:21], v[28:29]
	v_lshlrev_b32_e32 v20, 16, v23
	v_and_b32_e32 v21, 0xffff0000, v23
	v_pk_mul_f32 v[22:23], v[140:141], v[46:47] op_sel_hi:[0,1]
	v_pk_fma_f32 v[20:21], v[22:23], v[20:21], v[38:39]
	v_lshlrev_b32_e32 v22, 16, v27
	v_and_b32_e32 v23, 0xffff0000, v27
	v_pk_mul_f32 v[26:27], v[138:139], v[120:121] op_sel_hi:[0,1]
	v_pk_fma_f32 v[20:21], v[26:27], v[22:23], v[20:21]
	v_lshlrev_b32_e32 v22, 16, v31
	v_and_b32_e32 v23, 0xffff0000, v31
	v_pk_mul_f32 v[26:27], v[136:137], v[168:169] op_sel_hi:[0,1]
	v_pk_fma_f32 v[20:21], v[26:27], v[22:23], v[20:21]
	v_lshlrev_b32_e32 v22, 16, v35
	v_and_b32_e32 v23, 0xffff0000, v35
	v_pk_mul_f32 v[26:27], v[134:135], v[176:177] op_sel_hi:[0,1]
	v_pk_fma_f32 v[20:21], v[26:27], v[22:23], v[20:21]
	v_or_b32_e32 v139, 24, v141
	v_mul_f32_e32 v0, 0xbfb8aa3b, v20
	v_exp_f32_e32 v0, v0
	s_nop 0
	v_add_f32_e32 v0, 1.0, v0
	v_rcp_f32_e32 v22, v0
	v_mul_f32_e32 v0, 0xbfb8aa3b, v21
	v_exp_f32_e32 v0, v0
	s_nop 0
	v_add_f32_e32 v0, 1.0, v0
	v_rcp_f32_e32 v23, v0
	v_bfe_u32 v0, v40, 16, 1
	v_add3_u32 v0, v40, v0, s97
	v_pk_mul_f32 v[26:27], v[20:21], v[22:23]
	v_cvt_pk_bf16_f32 v20, v40, v41
	v_cvt_pk_bf16_f32 v21, v24, v25
	v_cvt_pk_bf16_f32 v22, v28, v29
	v_cvt_pk_bf16_f32 v23, v26, v27
	global_store_dwordx4 v[152:153], v[20:23], off offset:544
	s_nop 1
	v_mad_u32_u24 v20, v162, s66, v135
	ds_write_b16_d16_hi v20, v0 offset:34816
	v_bfe_u32 v0, v41, 16, 1
	v_add3_u32 v0, v41, v0, s97
	ds_write_b16_d16_hi v116, v0 offset:39440
	v_bfe_u32 v0, v24, 16, 1
	v_add3_u32 v0, v24, v0, s97
	ds_write_b16_d16_hi v116, v0 offset:39712
	v_bfe_u32 v0, v25, 16, 1
	v_add3_u32 v0, v25, v0, s97
	ds_write_b16_d16_hi v116, v0 offset:39984
	v_bfe_u32 v0, v28, 16, 1
	v_add3_u32 v0, v28, v0, s97
	ds_write_b16_d16_hi v116, v0 offset:40256
	v_bfe_u32 v0, v29, 16, 1
	v_add3_u32 v0, v29, v0, s97
	ds_write_b16_d16_hi v116, v0 offset:40528
	v_bfe_u32 v0, v26, 16, 1
	v_add3_u32 v0, v26, v0, s97
	ds_write_b16_d16_hi v116, v0 offset:40800
	v_bfe_u32 v0, v27, 16, 1
	v_add3_u32 v0, v27, v0, s97
	ds_write_b16_d16_hi v116, v0 offset:41072
	v_lshl_add_u64 v[40:41], v[144:145], 0, s[6:7]
	ds_read_b128 v[20:23], v215 offset:6768
	ds_read_b128 v[24:27], v215 offset:6752
	ds_read_b128 v[28:31], v215 offset:624
	ds_read_b128 v[32:35], v215 offset:608
	ds_read_b128 v[36:39], v215 offset:2160
	s_nop 0
	ds_read_b128 v[40:43], v215 offset:2144
	s_mov_b64 s[6:7], 0x1c60
	v_lshl_add_u64 v[48:49], v[144:145], 0, s[6:7]
	s_mov_b64 s[6:7], 0x2860
	ds_read_b128 v[44:47], v215 offset:3680
	s_nop 0
	ds_read_b128 v[48:51], v215 offset:3696
	v_lshl_add_u64 v[122:123], v[144:145], 0, s[6:7]
	ds_read_b128 v[118:121], v215 offset:5216
	s_nop 0
	ds_read_b128 v[122:125], v215 offset:5232
	s_mov_b64 s[6:7], 0x800
	v_lshl_add_u64 v[178:179], v[144:145], 0, s[6:7]
	s_mov_b64 s[6:7], 0x2000
	v_lshl_add_u64 v[186:187], v[144:145], 0, s[6:7]
	s_mov_b64 s[6:7], 0x2c00
	v_lshl_add_u64 v[194:195], v[144:145], 0, s[6:7]
	s_mov_b64 s[6:7], 0x820
	s_waitcnt lgkmcnt(0)
; __device__ __forceinline__ unsigned f2bf(float f) { unsigned u = __builtin_bit_cast(unsigned, f); return (u + 0x7fffu + ((u >> 16) & 1u)) >> 16; }
; DI unsigned pk2h(float lo, float hi) { const f32x2h_t v = {lo, hi}; return __builtin_bit_cast(unsigned, __builtin_convertvector(v, bf16x2h_t)); }
; DI float silu_f(float x) { return x * __builtin_amdgcn_rcpf(1.f + __expf(-x)); }
; DI void ssd_local_unit(Frame& F, int l, int ch, int g) {
;     ...
;     auto load_part = [&](const int part, v4u (&raw)[4][4]) {
; #pragma unroll
;         for (int cc = 0; cc < 4; ++cc)
; #pragma unroll
;             for (int j = 0; j < 4; ++j) raw[cc][j] = *(const v4u*)(proj + (size_t)(t0 + spc[j]) * PP + O_XBC + part * 256 + g * 128 + cg * 32 + cc * 8); };
;     auto do_part = [&](const int part, const v4u (&raw)[4][4]) {
; #pragma unroll
;         for (int cc = 0; cc < 4; ++cc) {
;             const int lc = cg * 32 + cc * 8, c0 = part * 256 + g * 128 + lc;
;             float acc[8];
;             { const f32x4 b0 = *(const f32x4*)(cb + c0), b1 = *(const f32x4*)(cb + c0 + 4);
; #pragma unroll
;               for (int e = 0; e < 4; ++e) { acc[e] = b0[e]; acc[4 + e] = b1[e]; } }
; #pragma unroll
;             for (int j = 0; j < 4; ++j) { float x[8]; unpack8(raw[cc][j], x);
;                 const f32x4 w0 = *(const f32x4*)(cw + j * XC + c0), w1 = *(const f32x4*)(cw + j * XC + c0 + 4);
; #pragma unroll
;                 for (int e = 0; e < 4; ++e) { acc[e] += w0[e] * okm[j] * x[e]; acc[4 + e] += w1[e] * okm[j] * x[4 + e]; } }
; #pragma unroll
;             for (int e = 0; e < 8; ++e) acc[e] = silu_f(acc[e]);
;             v4u o; o.x = pk2h(acc[0], acc[1]); o.y = pk2h(acc[2], acc[3]); o.z = pk2h(acc[4], acc[5]); o.w = pk2h(acc[6], acc[7]);
;             *(v4u*)(xbcc + (size_t)(t0 + s) * XC + c0) = o;
;             if (part == 0) { const int r2 = lc >> 6; const float dtv = DT[r2 * 128 + s], sc = dtv * __expf(AC[r2 * 128 + 127] - AC[r2 * 128 + s]);
; #pragma unroll
;                 for (int e = 0; e < 8; ++e) { XWT[(lc + e) * LP + s] = (bf16)f2bf(acc[e] * sc); XD[(lc + e) * LP + s] = (bf16)f2bf(acc[e] * dtv); } }
;             else if (part == 1) {
; #pragma unroll
;                 for (int e = 0; e < 8; ++e) BT[(lc + e) * LP + s] = (bf16)f2bf(acc[e]); }
	v_pk_mul_f32 v[32:33], v[140:141], v[32:33] op_sel_hi:[0,1]
	v_pk_fma_f32 v[24:25], v[32:33], v[126:127], v[24:25]
	v_lshlrev_b32_e32 v32, 16, v8
	v_and_b32_e32 v33, 0xffff0000, v8
	s_nop 0
	v_pk_mul_f32 v[40:41], v[138:139], v[40:41] op_sel_hi:[0,1]
	v_pk_fma_f32 v[24:25], v[40:41], v[32:33], v[24:25]
	v_lshlrev_b32_e32 v32, 16, v12
	v_and_b32_e32 v33, 0xffff0000, v12
	s_nop 0
	v_pk_mul_f32 v[40:41], v[136:137], v[44:45] op_sel_hi:[0,1]
	v_pk_fma_f32 v[24:25], v[40:41], v[32:33], v[24:25]
	v_lshlrev_b32_e32 v32, 16, v16
	v_and_b32_e32 v33, 0xffff0000, v16
	s_nop 0
	v_pk_mul_f32 v[40:41], v[134:135], v[118:119] op_sel_hi:[0,1]
	v_pk_fma_f32 v[24:25], v[40:41], v[32:33], v[24:25]
	v_lshlrev_b32_e32 v8, 16, v9
	v_mul_f32_e32 v0, 0xbfb8aa3b, v24
	v_exp_f32_e32 v0, v0
	v_and_b32_e32 v9, 0xffff0000, v9
	v_add_f32_e32 v0, 1.0, v0
	v_rcp_f32_e32 v32, v0
	v_mul_f32_e32 v0, 0xbfb8aa3b, v25
	v_exp_f32_e32 v0, v0
	s_nop 0
	v_add_f32_e32 v0, 1.0, v0
	v_rcp_f32_e32 v33, v0
	s_nop 0
	v_pk_mul_f32 v[24:25], v[24:25], v[32:33]
	v_pk_mul_f32 v[32:33], v[140:141], v[34:35] op_sel_hi:[0,1]
	v_pk_fma_f32 v[4:5], v[32:33], v[4:5], v[26:27]
	v_pk_mul_f32 v[26:27], v[138:139], v[42:43] op_sel_hi:[0,1]
	v_pk_fma_f32 v[4:5], v[26:27], v[8:9], v[4:5]
	v_lshlrev_b32_e32 v8, 16, v13
	v_and_b32_e32 v9, 0xffff0000, v13
	v_pk_mul_f32 v[12:13], v[136:137], v[46:47] op_sel_hi:[0,1]
	v_pk_fma_f32 v[4:5], v[12:13], v[8:9], v[4:5]
	v_lshlrev_b32_e32 v8, 16, v17
	v_and_b32_e32 v9, 0xffff0000, v17
	v_pk_mul_f32 v[12:13], v[134:135], v[120:121] op_sel_hi:[0,1]
	v_pk_fma_f32 v[4:5], v[12:13], v[8:9], v[4:5]
	v_pk_mul_f32 v[12:13], v[140:141], v[28:29] op_sel_hi:[0,1]
	v_mul_f32_e32 v0, 0xbfb8aa3b, v4
	v_exp_f32_e32 v0, v0
	v_pk_mul_f32 v[16:17], v[138:139], v[36:37] op_sel_hi:[0,1]
	v_add_f32_e32 v0, 1.0, v0
	v_rcp_f32_e32 v8, v0
	v_mul_f32_e32 v0, 0xbfb8aa3b, v5
	v_exp_f32_e32 v0, v0
	s_nop 0
	v_add_f32_e32 v0, 1.0, v0
	v_rcp_f32_e32 v9, v0
	s_nop 0
	v_pk_mul_f32 v[8:9], v[4:5], v[8:9]
	v_lshlrev_b32_e32 v4, 16, v6
	v_and_b32_e32 v5, 0xffff0000, v6
	v_pk_fma_f32 v[4:5], v[12:13], v[4:5], v[20:21]
	v_lshlrev_b32_e32 v12, 16, v10
	v_and_b32_e32 v13, 0xffff0000, v10
	v_pk_fma_f32 v[4:5], v[16:17], v[12:13], v[4:5]
	v_lshlrev_b32_e32 v12, 16, v14
	v_and_b32_e32 v13, 0xffff0000, v14
	v_pk_mul_f32 v[16:17], v[136:137], v[48:49] op_sel_hi:[0,1]
	v_pk_fma_f32 v[4:5], v[16:17], v[12:13], v[4:5]
	v_lshlrev_b32_e32 v12, 16, v18
	v_and_b32_e32 v13, 0xffff0000, v18
	s_nop 0
	v_pk_mul_f32 v[16:17], v[134:135], v[122:123] op_sel_hi:[0,1]
	v_pk_fma_f32 v[4:5], v[16:17], v[12:13], v[4:5]
	s_nop 0
	v_mul_f32_e32 v0, 0xbfb8aa3b, v4
	v_exp_f32_e32 v0, v0
	s_nop 0
	v_add_f32_e32 v0, 1.0, v0
	v_rcp_f32_e32 v12, v0
	v_mul_f32_e32 v0, 0xbfb8aa3b, v5
	v_exp_f32_e32 v0, v0
	s_nop 0
	v_add_f32_e32 v0, 1.0, v0
	v_rcp_f32_e32 v13, v0
	s_nop 0
	v_pk_mul_f32 v[12:13], v[4:5], v[12:13]
	v_lshlrev_b32_e32 v4, 16, v7
	v_and_b32_e32 v5, 0xffff0000, v7
	v_pk_mul_f32 v[6:7], v[140:141], v[30:31] op_sel_hi:[0,1]
	v_pk_fma_f32 v[4:5], v[6:7], v[4:5], v[22:23]
	v_lshlrev_b32_e32 v6, 16, v11
	v_and_b32_e32 v7, 0xffff0000, v11
	v_pk_mul_f32 v[10:11], v[138:139], v[38:39] op_sel_hi:[0,1]
	v_pk_fma_f32 v[4:5], v[10:11], v[6:7], v[4:5]
	v_lshlrev_b32_e32 v6, 16, v15
	v_and_b32_e32 v7, 0xffff0000, v15
	v_pk_mul_f32 v[10:11], v[136:137], v[50:51] op_sel_hi:[0,1]
	v_pk_fma_f32 v[4:5], v[10:11], v[6:7], v[4:5]
	v_lshlrev_b32_e32 v6, 16, v19
	v_and_b32_e32 v7, 0xffff0000, v19
	v_pk_mul_f32 v[10:11], v[134:135], v[124:125] op_sel_hi:[0,1]
	v_pk_fma_f32 v[4:5], v[10:11], v[6:7], v[4:5]
	s_nop 0
	v_mul_f32_e32 v0, 0xbfb8aa3b, v4
	v_exp_f32_e32 v0, v0
	s_nop 0
	v_add_f32_e32 v0, 1.0, v0
	v_rcp_f32_e32 v6, v0
	v_mul_f32_e32 v0, 0xbfb8aa3b, v5
	v_exp_f32_e32 v0, v0
	s_nop 0
	v_add_f32_e32 v0, 1.0, v0
	v_rcp_f32_e32 v7, v0
	v_bfe_u32 v0, v24, 16, 1
	v_add3_u32 v0, v24, v0, s97
	v_pk_mul_f32 v[10:11], v[4:5], v[6:7]
	v_cvt_pk_bf16_f32 v4, v24, v25
	v_cvt_pk_bf16_f32 v5, v8, v9
	v_cvt_pk_bf16_f32 v6, v12, v13
	v_cvt_pk_bf16_f32 v7, v10, v11
	global_store_dwordx4 v[152:153], v[4:7], off offset:560
	s_nop 1
	v_mad_u32_u24 v4, v139, s66, v135
	ds_write_b16_d16_hi v4, v0 offset:34816
	v_bfe_u32 v0, v25, 16, 1
	v_add3_u32 v0, v25, v0, s97
	ds_write_b16_d16_hi v116, v0 offset:41616
	v_bfe_u32 v0, v8, 16, 1
	v_add3_u32 v0, v8, v0, s97
	ds_write_b16_d16_hi v116, v0 offset:41888
	v_bfe_u32 v0, v9, 16, 1
	v_add3_u32 v0, v9, v0, s97
	ds_write_b16_d16_hi v116, v0 offset:42160
	v_bfe_u32 v0, v12, 16, 1
	v_add3_u32 v0, v12, v0, s97
	ds_write_b16_d16_hi v116, v0 offset:42432
	v_bfe_u32 v0, v13, 16, 1
	v_add3_u32 v0, v13, v0, s97
	ds_write_b16_d16_hi v116, v0 offset:42704
	v_bfe_u32 v0, v10, 16, 1
	v_add3_u32 v0, v10, v0, s97
	ds_write_b16_d16_hi v116, v0 offset:42976
	v_bfe_u32 v0, v11, 16, 1
	v_add3_u32 v0, v11, v0, s97
	ds_write_b16_d16_hi v116, v0 offset:43248
	global_load_dwordx4 v[4:7], v[154:155], off offset:3120
	global_load_dwordx4 v[20:23], v[154:155], off offset:3104
	global_load_dwordx4 v[36:39], v[154:155], off offset:3088
	global_load_dwordx4 v[116:119], v[154:155], off offset:3072
	global_load_dwordx4 v[8:11], v[156:157], off offset:3120
	global_load_dwordx4 v[24:27], v[156:157], off offset:3104
	global_load_dwordx4 v[40:43], v[156:157], off offset:3088
	global_load_dwordx4 v[120:123], v[156:157], off offset:3072
	global_load_dwordx4 v[12:15], v[158:159], off offset:3120
	global_load_dwordx4 v[28:31], v[158:159], off offset:3104
	global_load_dwordx4 v[44:47], v[158:159], off offset:3088
	global_load_dwordx4 v[124:127], v[158:159], off offset:3072
	global_load_dwordx4 v[16:19], v[160:161], off offset:3120
	global_load_dwordx4 v[32:35], v[160:161], off offset:3104
	global_load_dwordx4 v[48:51], v[160:161], off offset:3088
	global_load_dwordx4 v[128:131], v[160:161], off offset:3072
	ds_read_b128 v[154:157], v215 offset:7184
	s_nop 0
	ds_read_b128 v[158:161], v215 offset:7168
	ds_read_b128 v[166:169], v215 offset:1040
	ds_read_b128 v[170:173], v215 offset:1024
	ds_read_b128 v[174:177], v215 offset:2576
	s_nop 0
	ds_read_b128 v[178:181], v215 offset:2560
	s_nop 0
	ds_read_b128 v[182:185], v215 offset:4096
	s_nop 0
	ds_read_b128 v[186:189], v215 offset:4112
	s_nop 0
	ds_read_b128 v[190:193], v215 offset:5632
	s_nop 0
	ds_read_b128 v[194:197], v215 offset:5648
	s_waitcnt lgkmcnt(0)
; DI unsigned pk2h(float lo, float hi) { const f32x2h_t v = {lo, hi}; return __builtin_bit_cast(unsigned, __builtin_convertvector(v, bf16x2h_t)); }
; DI float silu_f(float x) { return x * __builtin_amdgcn_rcpf(1.f + __expf(-x)); }
; DI void ssd_local_unit(Frame& F, int l, int ch, int g) {
;     ...
;         for (int cc = 0; cc < 4; ++cc) {
;             const int lc = cg * 32 + cc * 8, c0 = part * 256 + g * 128 + lc;
;             float acc[8];
;             { const f32x4 b0 = *(const f32x4*)(cb + c0), b1 = *(const f32x4*)(cb + c0 + 4);
; #pragma unroll
;               for (int e = 0; e < 4; ++e) { acc[e] = b0[e]; acc[4 + e] = b1[e]; } }
; #pragma unroll
;             for (int j = 0; j < 4; ++j) { float x[8]; unpack8(raw[cc][j], x);
;                 const f32x4 w0 = *(const f32x4*)(cw + j * XC + c0), w1 = *(const f32x4*)(cw + j * XC + c0 + 4);
; #pragma unroll
;                 for (int e = 0; e < 4; ++e) { acc[e] += w0[e] * okm[j] * x[e]; acc[4 + e] += w1[e] * okm[j] * x[4 + e]; } }
; #pragma unroll
;             for (int e = 0; e < 8; ++e) acc[e] = silu_f(acc[e]);
;             v4u o; o.x = pk2h(acc[0], acc[1]); o.y = pk2h(acc[2], acc[3]); o.z = pk2h(acc[4], acc[5]); o.w = pk2h(acc[6], acc[7]);
;             *(v4u*)(xbcc + (size_t)(t0 + s) * XC + c0) = o;
	v_pk_mul_f32 v[170:171], v[140:141], v[170:171] op_sel_hi:[0,1]
	v_pk_fma_f32 v[158:159], v[170:171], v[198:199], v[158:159]
	v_lshlrev_b32_e32 v170, 16, v104
	v_and_b32_e32 v171, 0xffff0000, v104
	s_nop 0
	v_pk_mul_f32 v[178:179], v[138:139], v[178:179] op_sel_hi:[0,1]
	v_pk_fma_f32 v[158:159], v[178:179], v[170:171], v[158:159]
	v_lshlrev_b32_e32 v170, 16, v108
	v_and_b32_e32 v171, 0xffff0000, v108
	s_nop 0
	v_pk_mul_f32 v[178:179], v[136:137], v[182:183] op_sel_hi:[0,1]
	v_pk_fma_f32 v[158:159], v[178:179], v[170:171], v[158:159]
	v_lshlrev_b32_e32 v170, 16, v112
	v_and_b32_e32 v171, 0xffff0000, v112
	s_nop 0
	v_pk_mul_f32 v[178:179], v[134:135], v[190:191] op_sel_hi:[0,1]
	v_pk_fma_f32 v[158:159], v[178:179], v[170:171], v[158:159]
	v_lshlrev_b32_e32 v104, 16, v105
	v_mul_f32_e32 v0, 0xbfb8aa3b, v158
	v_exp_f32_e32 v0, v0
	v_and_b32_e32 v105, 0xffff0000, v105
	v_lshlrev_b32_e32 v182, 16, v84
	v_and_b32_e32 v183, 0xffff0000, v84
	v_add_f32_e32 v0, 1.0, v0
	v_rcp_f32_e32 v170, v0
	v_mul_f32_e32 v0, 0xbfb8aa3b, v159
	v_exp_f32_e32 v0, v0
	v_lshlrev_b32_e32 v84, 16, v85
	v_and_b32_e32 v85, 0xffff0000, v85
	v_add_f32_e32 v0, 1.0, v0
	v_rcp_f32_e32 v171, v0
	s_nop 0
	v_pk_mul_f32 v[158:159], v[158:159], v[170:171]
	v_pk_mul_f32 v[170:171], v[140:141], v[172:173] op_sel_hi:[0,1]
	v_pk_fma_f32 v[100:101], v[170:171], v[100:101], v[160:161]
	v_pk_mul_f32 v[160:161], v[138:139], v[180:181] op_sel_hi:[0,1]
	v_pk_fma_f32 v[100:101], v[160:161], v[104:105], v[100:101]
	v_lshlrev_b32_e32 v104, 16, v109
	v_and_b32_e32 v105, 0xffff0000, v109
	v_pk_mul_f32 v[108:109], v[136:137], v[184:185] op_sel_hi:[0,1]
	v_pk_fma_f32 v[100:101], v[108:109], v[104:105], v[100:101]
	v_lshlrev_b32_e32 v104, 16, v113
	v_and_b32_e32 v105, 0xffff0000, v113
	v_pk_mul_f32 v[108:109], v[134:135], v[192:193] op_sel_hi:[0,1]
	v_pk_fma_f32 v[100:101], v[108:109], v[104:105], v[100:101]
	v_pk_mul_f32 v[108:109], v[140:141], v[166:167] op_sel_hi:[0,1]
	v_mul_f32_e32 v0, 0xbfb8aa3b, v100
	v_exp_f32_e32 v0, v0
	v_pk_mul_f32 v[112:113], v[138:139], v[174:175] op_sel_hi:[0,1]
	v_add_f32_e32 v0, 1.0, v0
	v_rcp_f32_e32 v104, v0
	v_mul_f32_e32 v0, 0xbfb8aa3b, v101
	v_exp_f32_e32 v0, v0
	s_nop 0
	v_add_f32_e32 v0, 1.0, v0
	v_rcp_f32_e32 v105, v0
	s_nop 0
	v_pk_mul_f32 v[104:105], v[100:101], v[104:105]
	v_lshlrev_b32_e32 v100, 16, v102
	v_and_b32_e32 v101, 0xffff0000, v102
	v_pk_fma_f32 v[100:101], v[108:109], v[100:101], v[154:155]
	v_lshlrev_b32_e32 v108, 16, v106
	v_and_b32_e32 v109, 0xffff0000, v106
	v_pk_fma_f32 v[100:101], v[112:113], v[108:109], v[100:101]
	v_lshlrev_b32_e32 v108, 16, v110
	v_and_b32_e32 v109, 0xffff0000, v110
	v_pk_mul_f32 v[112:113], v[136:137], v[186:187] op_sel_hi:[0,1]
	v_pk_fma_f32 v[100:101], v[112:113], v[108:109], v[100:101]
	v_lshlrev_b32_e32 v108, 16, v114
	v_and_b32_e32 v109, 0xffff0000, v114
	s_waitcnt vmcnt(0)
	v_pk_mul_f32 v[112:113], v[134:135], v[194:195] op_sel_hi:[0,1]
	v_pk_fma_f32 v[100:101], v[112:113], v[108:109], v[100:101]
	s_nop 0
	v_mul_f32_e32 v0, 0xbfb8aa3b, v100
	v_exp_f32_e32 v0, v0
	s_nop 0
	v_add_f32_e32 v0, 1.0, v0
	v_rcp_f32_e32 v108, v0
	v_mul_f32_e32 v0, 0xbfb8aa3b, v101
	v_exp_f32_e32 v0, v0
	s_nop 0
	v_add_f32_e32 v0, 1.0, v0
	v_rcp_f32_e32 v109, v0
	s_nop 0
	v_pk_mul_f32 v[108:109], v[100:101], v[108:109]
	v_lshlrev_b32_e32 v100, 16, v103
	v_and_b32_e32 v101, 0xffff0000, v103
	v_pk_mul_f32 v[102:103], v[140:141], v[168:169] op_sel_hi:[0,1]
	v_pk_fma_f32 v[100:101], v[102:103], v[100:101], v[156:157]
	v_lshlrev_b32_e32 v102, 16, v107
	v_and_b32_e32 v103, 0xffff0000, v107
	v_pk_mul_f32 v[106:107], v[138:139], v[176:177] op_sel_hi:[0,1]
	v_pk_fma_f32 v[100:101], v[106:107], v[102:103], v[100:101]
	v_lshlrev_b32_e32 v102, 16, v111
	v_and_b32_e32 v103, 0xffff0000, v111
	v_pk_mul_f32 v[106:107], v[136:137], v[188:189] op_sel_hi:[0,1]
	v_pk_fma_f32 v[100:101], v[106:107], v[102:103], v[100:101]
	v_lshlrev_b32_e32 v102, 16, v115
	v_and_b32_e32 v103, 0xffff0000, v115
	v_pk_mul_f32 v[106:107], v[134:135], v[196:197] op_sel_hi:[0,1]
	v_pk_fma_f32 v[100:101], v[106:107], v[102:103], v[100:101]
	s_nop 0
	v_mul_f32_e32 v0, 0xbfb8aa3b, v100
	v_exp_f32_e32 v0, v0
	s_nop 0
	v_add_f32_e32 v0, 1.0, v0
	v_rcp_f32_e32 v102, v0
	v_mul_f32_e32 v0, 0xbfb8aa3b, v101
	v_exp_f32_e32 v0, v0
	s_nop 0
	v_add_f32_e32 v0, 1.0, v0
	v_rcp_f32_e32 v103, v0
	s_nop 0
	v_pk_mul_f32 v[106:107], v[100:101], v[102:103]
	v_cvt_pk_bf16_f32 v100, v158, v159
	v_cvt_pk_bf16_f32 v101, v104, v105
	v_cvt_pk_bf16_f32 v102, v108, v109
	v_cvt_pk_bf16_f32 v103, v106, v107
	global_store_dwordx4 v[152:153], v[100:103], off offset:1024
	v_lshl_add_u64 v[158:159], v[144:145], 0, s[6:7]
	ds_read_b128 v[100:103], v215 offset:7216
	ds_read_b128 v[104:107], v215 offset:7200
	ds_read_b128 v[108:111], v215 offset:1072
	ds_read_b128 v[112:115], v215 offset:1056
	ds_read_b128 v[154:157], v215 offset:2608
	s_nop 0
	ds_read_b128 v[158:161], v215 offset:2592
	s_mov_b64 s[6:7], 0x2020
	v_lshl_add_u64 v[170:171], v[144:145], 0, s[6:7]
	s_mov_b64 s[6:7], 0x2c20
	ds_read_b128 v[166:169], v215 offset:4128
	s_nop 0
	ds_read_b128 v[170:173], v215 offset:4144
	v_lshl_add_u64 v[178:179], v[144:145], 0, s[6:7]
	ds_read_b128 v[174:177], v215 offset:5664
	s_nop 0
	ds_read_b128 v[178:181], v215 offset:5680
	s_mov_b64 s[6:7], 0x840
	s_waitcnt lgkmcnt(0)
; DI unsigned pk2h(float lo, float hi) { const f32x2h_t v = {lo, hi}; return __builtin_bit_cast(unsigned, __builtin_convertvector(v, bf16x2h_t)); }
; DI float silu_f(float x) { return x * __builtin_amdgcn_rcpf(1.f + __expf(-x)); }
; DI void ssd_local_unit(Frame& F, int l, int ch, int g) {
;     ...
;         for (int cc = 0; cc < 4; ++cc) {
;             const int lc = cg * 32 + cc * 8, c0 = part * 256 + g * 128 + lc;
;             float acc[8];
;             { const f32x4 b0 = *(const f32x4*)(cb + c0), b1 = *(const f32x4*)(cb + c0 + 4);
; #pragma unroll
;               for (int e = 0; e < 4; ++e) { acc[e] = b0[e]; acc[4 + e] = b1[e]; } }
; #pragma unroll
;             for (int j = 0; j < 4; ++j) { float x[8]; unpack8(raw[cc][j], x);
;                 const f32x4 w0 = *(const f32x4*)(cw + j * XC + c0), w1 = *(const f32x4*)(cw + j * XC + c0 + 4);
; #pragma unroll
;                 for (int e = 0; e < 4; ++e) { acc[e] += w0[e] * okm[j] * x[e]; acc[4 + e] += w1[e] * okm[j] * x[4 + e]; } }
; #pragma unroll
;             for (int e = 0; e < 8; ++e) acc[e] = silu_f(acc[e]);
;             v4u o; o.x = pk2h(acc[0], acc[1]); o.y = pk2h(acc[2], acc[3]); o.z = pk2h(acc[4], acc[5]); o.w = pk2h(acc[6], acc[7]);
;             *(v4u*)(xbcc + (size_t)(t0 + s) * XC + c0) = o;
	v_pk_mul_f32 v[112:113], v[140:141], v[112:113] op_sel_hi:[0,1]
	v_pk_fma_f32 v[104:105], v[112:113], v[182:183], v[104:105]
	v_lshlrev_b32_e32 v112, 16, v88
	v_and_b32_e32 v113, 0xffff0000, v88
	s_nop 0
	v_pk_mul_f32 v[158:159], v[138:139], v[158:159] op_sel_hi:[0,1]
	v_pk_fma_f32 v[104:105], v[158:159], v[112:113], v[104:105]
	v_lshlrev_b32_e32 v112, 16, v92
	v_and_b32_e32 v113, 0xffff0000, v92
	s_nop 0
	v_pk_mul_f32 v[158:159], v[136:137], v[166:167] op_sel_hi:[0,1]
	v_pk_fma_f32 v[104:105], v[158:159], v[112:113], v[104:105]
	v_lshlrev_b32_e32 v112, 16, v96
	v_and_b32_e32 v113, 0xffff0000, v96
	s_nop 0
	v_pk_mul_f32 v[158:159], v[134:135], v[174:175] op_sel_hi:[0,1]
	v_pk_fma_f32 v[104:105], v[158:159], v[112:113], v[104:105]
	v_lshlrev_b32_e32 v88, 16, v89
	v_mul_f32_e32 v0, 0xbfb8aa3b, v104
	v_exp_f32_e32 v0, v0
	v_and_b32_e32 v89, 0xffff0000, v89
	v_lshlrev_b32_e32 v166, 16, v68
	v_and_b32_e32 v167, 0xffff0000, v68
	v_add_f32_e32 v0, 1.0, v0
	v_rcp_f32_e32 v112, v0
	v_mul_f32_e32 v0, 0xbfb8aa3b, v105
	v_exp_f32_e32 v0, v0
	v_lshlrev_b32_e32 v68, 16, v69
	v_and_b32_e32 v69, 0xffff0000, v69
	v_add_f32_e32 v0, 1.0, v0
	v_rcp_f32_e32 v113, v0
	s_nop 0
	v_pk_mul_f32 v[104:105], v[104:105], v[112:113]
	v_pk_mul_f32 v[112:113], v[140:141], v[114:115] op_sel_hi:[0,1]
	v_pk_fma_f32 v[84:85], v[112:113], v[84:85], v[106:107]
	v_pk_mul_f32 v[106:107], v[138:139], v[160:161] op_sel_hi:[0,1]
	v_pk_fma_f32 v[84:85], v[106:107], v[88:89], v[84:85]
	v_lshlrev_b32_e32 v88, 16, v93
	v_and_b32_e32 v89, 0xffff0000, v93
	v_pk_mul_f32 v[92:93], v[136:137], v[168:169] op_sel_hi:[0,1]
	v_pk_fma_f32 v[84:85], v[92:93], v[88:89], v[84:85]
	v_lshlrev_b32_e32 v88, 16, v97
	v_and_b32_e32 v89, 0xffff0000, v97
	v_pk_mul_f32 v[92:93], v[134:135], v[176:177] op_sel_hi:[0,1]
	v_pk_fma_f32 v[84:85], v[92:93], v[88:89], v[84:85]
	v_pk_mul_f32 v[92:93], v[140:141], v[108:109] op_sel_hi:[0,1]
	v_mul_f32_e32 v0, 0xbfb8aa3b, v84
	v_exp_f32_e32 v0, v0
	v_pk_mul_f32 v[96:97], v[138:139], v[154:155] op_sel_hi:[0,1]
	v_add_f32_e32 v0, 1.0, v0
	v_rcp_f32_e32 v88, v0
	v_mul_f32_e32 v0, 0xbfb8aa3b, v85
	v_exp_f32_e32 v0, v0
	s_nop 0
	v_add_f32_e32 v0, 1.0, v0
	v_rcp_f32_e32 v89, v0
	s_nop 0
	v_pk_mul_f32 v[88:89], v[84:85], v[88:89]
	v_lshlrev_b32_e32 v84, 16, v86
	v_and_b32_e32 v85, 0xffff0000, v86
	v_pk_fma_f32 v[84:85], v[92:93], v[84:85], v[100:101]
	v_lshlrev_b32_e32 v92, 16, v90
	v_and_b32_e32 v93, 0xffff0000, v90
	v_pk_fma_f32 v[84:85], v[96:97], v[92:93], v[84:85]
	v_lshlrev_b32_e32 v92, 16, v94
	v_and_b32_e32 v93, 0xffff0000, v94
	v_pk_mul_f32 v[96:97], v[136:137], v[170:171] op_sel_hi:[0,1]
	v_pk_fma_f32 v[84:85], v[96:97], v[92:93], v[84:85]
	v_lshlrev_b32_e32 v92, 16, v98
	v_and_b32_e32 v93, 0xffff0000, v98
	s_nop 0
	v_pk_mul_f32 v[96:97], v[134:135], v[178:179] op_sel_hi:[0,1]
	v_pk_fma_f32 v[84:85], v[96:97], v[92:93], v[84:85]
	s_nop 0
	v_mul_f32_e32 v0, 0xbfb8aa3b, v84
	v_exp_f32_e32 v0, v0
	s_nop 0
	v_add_f32_e32 v0, 1.0, v0
	v_rcp_f32_e32 v92, v0
	v_mul_f32_e32 v0, 0xbfb8aa3b, v85
	v_exp_f32_e32 v0, v0
	s_nop 0
	v_add_f32_e32 v0, 1.0, v0
	v_rcp_f32_e32 v93, v0
	s_nop 0
	v_pk_mul_f32 v[92:93], v[84:85], v[92:93]
	v_lshlrev_b32_e32 v84, 16, v87
	v_and_b32_e32 v85, 0xffff0000, v87
	v_pk_mul_f32 v[86:87], v[140:141], v[110:111] op_sel_hi:[0,1]
	v_pk_fma_f32 v[84:85], v[86:87], v[84:85], v[102:103]
	v_lshlrev_b32_e32 v86, 16, v91
	v_and_b32_e32 v87, 0xffff0000, v91
	v_pk_mul_f32 v[90:91], v[138:139], v[156:157] op_sel_hi:[0,1]
	v_pk_fma_f32 v[84:85], v[90:91], v[86:87], v[84:85]
	v_lshlrev_b32_e32 v86, 16, v95
	v_and_b32_e32 v87, 0xffff0000, v95
	v_pk_mul_f32 v[90:91], v[136:137], v[172:173] op_sel_hi:[0,1]
	v_pk_fma_f32 v[84:85], v[90:91], v[86:87], v[84:85]
	v_lshlrev_b32_e32 v86, 16, v99
	v_and_b32_e32 v87, 0xffff0000, v99
	v_pk_mul_f32 v[90:91], v[134:135], v[180:181] op_sel_hi:[0,1]
	v_pk_fma_f32 v[84:85], v[90:91], v[86:87], v[84:85]
	s_nop 0
	v_mul_f32_e32 v0, 0xbfb8aa3b, v84
	v_exp_f32_e32 v0, v0
	s_nop 0
	v_add_f32_e32 v0, 1.0, v0
	v_rcp_f32_e32 v86, v0
	v_mul_f32_e32 v0, 0xbfb8aa3b, v85
	v_exp_f32_e32 v0, v0
	s_nop 0
	v_add_f32_e32 v0, 1.0, v0
	v_rcp_f32_e32 v87, v0
	s_nop 0
	v_pk_mul_f32 v[90:91], v[84:85], v[86:87]
	v_cvt_pk_bf16_f32 v84, v104, v105
	v_cvt_pk_bf16_f32 v85, v88, v89
	v_cvt_pk_bf16_f32 v86, v92, v93
	v_cvt_pk_bf16_f32 v87, v90, v91
	global_store_dwordx4 v[152:153], v[84:87], off offset:1040
	v_lshl_add_u64 v[104:105], v[144:145], 0, s[6:7]
	ds_read_b128 v[84:87], v215 offset:7248
	ds_read_b128 v[88:91], v215 offset:7232
	ds_read_b128 v[92:95], v215 offset:1104
	ds_read_b128 v[96:99], v215 offset:1088
	ds_read_b128 v[100:103], v215 offset:2640
	s_nop 0
	ds_read_b128 v[104:107], v215 offset:2624
	s_mov_b64 s[6:7], 0x2040
	v_lshl_add_u64 v[112:113], v[144:145], 0, s[6:7]
	s_mov_b64 s[6:7], 0x2c40
	ds_read_b128 v[108:111], v215 offset:4160
	s_nop 0
	ds_read_b128 v[112:115], v215 offset:4176
	v_lshl_add_u64 v[158:159], v[144:145], 0, s[6:7]
	ds_read_b128 v[154:157], v215 offset:5696
	s_nop 0
	ds_read_b128 v[158:161], v215 offset:5712
	s_mov_b64 s[6:7], 0x860
	s_waitcnt lgkmcnt(0)
; DI unsigned pk2h(float lo, float hi) { const f32x2h_t v = {lo, hi}; return __builtin_bit_cast(unsigned, __builtin_convertvector(v, bf16x2h_t)); }
; DI float silu_f(float x) { return x * __builtin_amdgcn_rcpf(1.f + __expf(-x)); }
; DI void ssd_local_unit(Frame& F, int l, int ch, int g) {
;     ...
;         for (int cc = 0; cc < 4; ++cc) {
;             const int lc = cg * 32 + cc * 8, c0 = part * 256 + g * 128 + lc;
;             float acc[8];
;             { const f32x4 b0 = *(const f32x4*)(cb + c0), b1 = *(const f32x4*)(cb + c0 + 4);
; #pragma unroll
;               for (int e = 0; e < 4; ++e) { acc[e] = b0[e]; acc[4 + e] = b1[e]; } }
; #pragma unroll
;             for (int j = 0; j < 4; ++j) { float x[8]; unpack8(raw[cc][j], x);
;                 const f32x4 w0 = *(const f32x4*)(cw + j * XC + c0), w1 = *(const f32x4*)(cw + j * XC + c0 + 4);
; #pragma unroll
;                 for (int e = 0; e < 4; ++e) { acc[e] += w0[e] * okm[j] * x[e]; acc[4 + e] += w1[e] * okm[j] * x[4 + e]; } }
; #pragma unroll
;             for (int e = 0; e < 8; ++e) acc[e] = silu_f(acc[e]);
;             v4u o; o.x = pk2h(acc[0], acc[1]); o.y = pk2h(acc[2], acc[3]); o.z = pk2h(acc[4], acc[5]); o.w = pk2h(acc[6], acc[7]);
;             *(v4u*)(xbcc + (size_t)(t0 + s) * XC + c0) = o;
	v_pk_mul_f32 v[96:97], v[140:141], v[96:97] op_sel_hi:[0,1]
	v_pk_fma_f32 v[88:89], v[96:97], v[166:167], v[88:89]
	v_lshlrev_b32_e32 v96, 16, v72
	v_and_b32_e32 v97, 0xffff0000, v72
	s_nop 0
	v_pk_mul_f32 v[104:105], v[138:139], v[104:105] op_sel_hi:[0,1]
	v_pk_fma_f32 v[88:89], v[104:105], v[96:97], v[88:89]
	v_lshlrev_b32_e32 v96, 16, v76
	v_and_b32_e32 v97, 0xffff0000, v76
	s_nop 0
	v_pk_mul_f32 v[104:105], v[136:137], v[108:109] op_sel_hi:[0,1]
	v_pk_fma_f32 v[88:89], v[104:105], v[96:97], v[88:89]
	v_lshlrev_b32_e32 v96, 16, v80
	v_and_b32_e32 v97, 0xffff0000, v80
	s_nop 0
	v_pk_mul_f32 v[104:105], v[134:135], v[154:155] op_sel_hi:[0,1]
	v_pk_fma_f32 v[88:89], v[104:105], v[96:97], v[88:89]
	v_lshlrev_b32_e32 v72, 16, v73
	v_mul_f32_e32 v0, 0xbfb8aa3b, v88
	v_exp_f32_e32 v0, v0
	v_and_b32_e32 v73, 0xffff0000, v73
	v_lshlrev_b32_e32 v108, 16, v52
	v_and_b32_e32 v109, 0xffff0000, v52
	v_add_f32_e32 v0, 1.0, v0
	v_rcp_f32_e32 v96, v0
	v_mul_f32_e32 v0, 0xbfb8aa3b, v89
	v_exp_f32_e32 v0, v0
	v_lshlrev_b32_e32 v52, 16, v53
	v_and_b32_e32 v53, 0xffff0000, v53
	v_add_f32_e32 v0, 1.0, v0
	v_rcp_f32_e32 v97, v0
	s_nop 0
	v_pk_mul_f32 v[88:89], v[88:89], v[96:97]
	v_pk_mul_f32 v[96:97], v[140:141], v[98:99] op_sel_hi:[0,1]
	v_pk_fma_f32 v[68:69], v[96:97], v[68:69], v[90:91]
	v_pk_mul_f32 v[90:91], v[138:139], v[106:107] op_sel_hi:[0,1]
	v_pk_fma_f32 v[68:69], v[90:91], v[72:73], v[68:69]
	v_lshlrev_b32_e32 v72, 16, v77
	v_and_b32_e32 v73, 0xffff0000, v77
	v_pk_mul_f32 v[76:77], v[136:137], v[110:111] op_sel_hi:[0,1]
	v_pk_fma_f32 v[68:69], v[76:77], v[72:73], v[68:69]
	v_lshlrev_b32_e32 v72, 16, v81
	v_and_b32_e32 v73, 0xffff0000, v81
	v_pk_mul_f32 v[76:77], v[134:135], v[156:157] op_sel_hi:[0,1]
	v_pk_fma_f32 v[68:69], v[76:77], v[72:73], v[68:69]
	v_pk_mul_f32 v[76:77], v[140:141], v[92:93] op_sel_hi:[0,1]
	v_mul_f32_e32 v0, 0xbfb8aa3b, v68
	v_exp_f32_e32 v0, v0
	v_pk_mul_f32 v[80:81], v[138:139], v[100:101] op_sel_hi:[0,1]
	v_add_f32_e32 v0, 1.0, v0
	v_rcp_f32_e32 v72, v0
	v_mul_f32_e32 v0, 0xbfb8aa3b, v69
	v_exp_f32_e32 v0, v0
	s_nop 0
	v_add_f32_e32 v0, 1.0, v0
	v_rcp_f32_e32 v73, v0
	s_nop 0
	v_pk_mul_f32 v[72:73], v[68:69], v[72:73]
	v_lshlrev_b32_e32 v68, 16, v70
	v_and_b32_e32 v69, 0xffff0000, v70
	v_pk_fma_f32 v[68:69], v[76:77], v[68:69], v[84:85]
	v_lshlrev_b32_e32 v76, 16, v74
	v_and_b32_e32 v77, 0xffff0000, v74
	v_pk_fma_f32 v[68:69], v[80:81], v[76:77], v[68:69]
	v_lshlrev_b32_e32 v76, 16, v78
	v_and_b32_e32 v77, 0xffff0000, v78
	v_pk_mul_f32 v[80:81], v[136:137], v[112:113] op_sel_hi:[0,1]
	v_pk_fma_f32 v[68:69], v[80:81], v[76:77], v[68:69]
	v_lshlrev_b32_e32 v76, 16, v82
	v_and_b32_e32 v77, 0xffff0000, v82
	s_nop 0
	v_pk_mul_f32 v[80:81], v[134:135], v[158:159] op_sel_hi:[0,1]
	v_pk_fma_f32 v[68:69], v[80:81], v[76:77], v[68:69]
	s_nop 0
	v_mul_f32_e32 v0, 0xbfb8aa3b, v68
	v_exp_f32_e32 v0, v0
	s_nop 0
	v_add_f32_e32 v0, 1.0, v0
	v_rcp_f32_e32 v76, v0
	v_mul_f32_e32 v0, 0xbfb8aa3b, v69
	v_exp_f32_e32 v0, v0
	s_nop 0
	v_add_f32_e32 v0, 1.0, v0
	v_rcp_f32_e32 v77, v0
	s_nop 0
	v_pk_mul_f32 v[76:77], v[68:69], v[76:77]
	v_lshlrev_b32_e32 v68, 16, v71
	v_and_b32_e32 v69, 0xffff0000, v71
	v_pk_mul_f32 v[70:71], v[140:141], v[94:95] op_sel_hi:[0,1]
	v_pk_fma_f32 v[68:69], v[70:71], v[68:69], v[86:87]
	v_lshlrev_b32_e32 v70, 16, v75
	v_and_b32_e32 v71, 0xffff0000, v75
	v_pk_mul_f32 v[74:75], v[138:139], v[102:103] op_sel_hi:[0,1]
	v_pk_fma_f32 v[68:69], v[74:75], v[70:71], v[68:69]
	v_lshlrev_b32_e32 v70, 16, v79
	v_and_b32_e32 v71, 0xffff0000, v79
	v_pk_mul_f32 v[74:75], v[136:137], v[114:115] op_sel_hi:[0,1]
	v_pk_fma_f32 v[68:69], v[74:75], v[70:71], v[68:69]
	v_lshlrev_b32_e32 v70, 16, v83
	v_and_b32_e32 v71, 0xffff0000, v83
	v_pk_mul_f32 v[74:75], v[134:135], v[160:161] op_sel_hi:[0,1]
	v_pk_fma_f32 v[68:69], v[74:75], v[70:71], v[68:69]
	s_nop 0
	v_mul_f32_e32 v0, 0xbfb8aa3b, v68
	v_exp_f32_e32 v0, v0
	s_nop 0
	v_add_f32_e32 v0, 1.0, v0
	v_rcp_f32_e32 v70, v0
	v_mul_f32_e32 v0, 0xbfb8aa3b, v69
	v_exp_f32_e32 v0, v0
	s_nop 0
	v_add_f32_e32 v0, 1.0, v0
	v_rcp_f32_e32 v71, v0
	s_nop 0
	v_pk_mul_f32 v[74:75], v[68:69], v[70:71]
	v_cvt_pk_bf16_f32 v68, v88, v89
	v_cvt_pk_bf16_f32 v69, v72, v73
	v_cvt_pk_bf16_f32 v70, v76, v77
	v_cvt_pk_bf16_f32 v71, v74, v75
	global_store_dwordx4 v[152:153], v[68:71], off offset:1056
	v_lshl_add_u64 v[88:89], v[144:145], 0, s[6:7]
	ds_read_b128 v[68:71], v215 offset:7280
	ds_read_b128 v[72:75], v215 offset:7264
	ds_read_b128 v[76:79], v215 offset:1136
	ds_read_b128 v[80:83], v215 offset:1120
	ds_read_b128 v[84:87], v215 offset:2672
	s_nop 0
	ds_read_b128 v[88:91], v215 offset:2656
	s_mov_b64 s[6:7], 0x2060
	v_lshl_add_u64 v[96:97], v[144:145], 0, s[6:7]
	s_mov_b64 s[6:7], 0x2c60
	ds_read_b128 v[92:95], v215 offset:4192
	s_nop 0
	ds_read_b128 v[96:99], v215 offset:4208
	v_lshl_add_u64 v[104:105], v[144:145], 0, s[6:7]
	ds_read_b128 v[100:103], v215 offset:5728
	s_nop 0
	ds_read_b128 v[104:107], v215 offset:5744
	s_mov_b64 s[6:7], 0x1800
	s_waitcnt lgkmcnt(0)
; DI unsigned pk2h(float lo, float hi) { const f32x2h_t v = {lo, hi}; return __builtin_bit_cast(unsigned, __builtin_convertvector(v, bf16x2h_t)); }
; DI float silu_f(float x) { return x * __builtin_amdgcn_rcpf(1.f + __expf(-x)); }
; DI void ssd_local_unit(Frame& F, int l, int ch, int g) {
;     ...
;         for (int cc = 0; cc < 4; ++cc) {
;             const int lc = cg * 32 + cc * 8, c0 = part * 256 + g * 128 + lc;
;             float acc[8];
;             { const f32x4 b0 = *(const f32x4*)(cb + c0), b1 = *(const f32x4*)(cb + c0 + 4);
; #pragma unroll
;               for (int e = 0; e < 4; ++e) { acc[e] = b0[e]; acc[4 + e] = b1[e]; } }
; #pragma unroll
;             for (int j = 0; j < 4; ++j) { float x[8]; unpack8(raw[cc][j], x);
;                 const f32x4 w0 = *(const f32x4*)(cw + j * XC + c0), w1 = *(const f32x4*)(cw + j * XC + c0 + 4);
; #pragma unroll
;                 for (int e = 0; e < 4; ++e) { acc[e] += w0[e] * okm[j] * x[e]; acc[4 + e] += w1[e] * okm[j] * x[4 + e]; } }
; #pragma unroll
;             for (int e = 0; e < 8; ++e) acc[e] = silu_f(acc[e]);
;             v4u o; o.x = pk2h(acc[0], acc[1]); o.y = pk2h(acc[2], acc[3]); o.z = pk2h(acc[4], acc[5]); o.w = pk2h(acc[6], acc[7]);
;             *(v4u*)(xbcc + (size_t)(t0 + s) * XC + c0) = o;
	v_pk_mul_f32 v[80:81], v[140:141], v[80:81] op_sel_hi:[0,1]
	v_pk_fma_f32 v[72:73], v[80:81], v[108:109], v[72:73]
	v_lshlrev_b32_e32 v80, 16, v56
	v_and_b32_e32 v81, 0xffff0000, v56
	s_nop 0
	v_pk_mul_f32 v[88:89], v[138:139], v[88:89] op_sel_hi:[0,1]
	v_pk_fma_f32 v[72:73], v[88:89], v[80:81], v[72:73]
	v_lshlrev_b32_e32 v80, 16, v60
	v_and_b32_e32 v81, 0xffff0000, v60
	s_nop 0
	v_pk_mul_f32 v[88:89], v[136:137], v[92:93] op_sel_hi:[0,1]
	v_pk_fma_f32 v[72:73], v[88:89], v[80:81], v[72:73]
	v_lshlrev_b32_e32 v80, 16, v64
	v_and_b32_e32 v81, 0xffff0000, v64
	s_nop 0
	v_pk_mul_f32 v[88:89], v[134:135], v[100:101] op_sel_hi:[0,1]
	v_pk_fma_f32 v[72:73], v[88:89], v[80:81], v[72:73]
	v_lshlrev_b32_e32 v56, 16, v57
	v_mul_f32_e32 v0, 0xbfb8aa3b, v72
	v_exp_f32_e32 v0, v0
	v_and_b32_e32 v57, 0xffff0000, v57
	v_lshlrev_b32_e32 v92, 16, v116
	v_and_b32_e32 v93, 0xffff0000, v116
	v_add_f32_e32 v0, 1.0, v0
	v_rcp_f32_e32 v80, v0
	v_mul_f32_e32 v0, 0xbfb8aa3b, v73
	v_exp_f32_e32 v0, v0
	s_nop 0
	v_add_f32_e32 v0, 1.0, v0
	v_rcp_f32_e32 v81, v0
	s_nop 0
	v_pk_mul_f32 v[72:73], v[72:73], v[80:81]
	v_pk_mul_f32 v[80:81], v[140:141], v[82:83] op_sel_hi:[0,1]
	v_pk_fma_f32 v[52:53], v[80:81], v[52:53], v[74:75]
	v_pk_mul_f32 v[74:75], v[138:139], v[90:91] op_sel_hi:[0,1]
	v_pk_fma_f32 v[52:53], v[74:75], v[56:57], v[52:53]
	v_lshlrev_b32_e32 v56, 16, v61
	v_and_b32_e32 v57, 0xffff0000, v61
	v_pk_mul_f32 v[60:61], v[136:137], v[94:95] op_sel_hi:[0,1]
	v_pk_fma_f32 v[52:53], v[60:61], v[56:57], v[52:53]
	v_lshlrev_b32_e32 v56, 16, v65
	v_and_b32_e32 v57, 0xffff0000, v65
	v_pk_mul_f32 v[60:61], v[134:135], v[102:103] op_sel_hi:[0,1]
	v_pk_fma_f32 v[52:53], v[60:61], v[56:57], v[52:53]
	v_pk_mul_f32 v[60:61], v[140:141], v[76:77] op_sel_hi:[0,1]
	v_mul_f32_e32 v0, 0xbfb8aa3b, v52
	v_exp_f32_e32 v0, v0
	v_pk_mul_f32 v[64:65], v[138:139], v[84:85] op_sel_hi:[0,1]
	v_lshl_add_u64 v[80:81], v[144:145], 0, s[6:7]
	s_mov_b64 s[6:7], 0x2400
	v_add_f32_e32 v0, 1.0, v0
	v_rcp_f32_e32 v56, v0
	v_mul_f32_e32 v0, 0xbfb8aa3b, v53
	v_exp_f32_e32 v0, v0
	v_lshl_add_u64 v[88:89], v[144:145], 0, s[6:7]
	s_movk_i32 s6, 0x2000
	v_add_f32_e32 v0, 1.0, v0
	v_rcp_f32_e32 v57, v0
	s_nop 0
	v_pk_mul_f32 v[56:57], v[52:53], v[56:57]
	v_lshlrev_b32_e32 v52, 16, v54
	v_and_b32_e32 v53, 0xffff0000, v54
	v_pk_fma_f32 v[52:53], v[60:61], v[52:53], v[68:69]
	v_lshlrev_b32_e32 v60, 16, v58
	v_and_b32_e32 v61, 0xffff0000, v58
	v_pk_fma_f32 v[52:53], v[64:65], v[60:61], v[52:53]
	v_lshlrev_b32_e32 v60, 16, v62
	v_and_b32_e32 v61, 0xffff0000, v62
	v_pk_mul_f32 v[64:65], v[136:137], v[96:97] op_sel_hi:[0,1]
	v_pk_fma_f32 v[52:53], v[64:65], v[60:61], v[52:53]
	v_lshlrev_b32_e32 v60, 16, v66
	v_and_b32_e32 v61, 0xffff0000, v66
	s_nop 0
	v_pk_mul_f32 v[64:65], v[134:135], v[104:105] op_sel_hi:[0,1]
	v_pk_fma_f32 v[52:53], v[64:65], v[60:61], v[52:53]
	s_nop 0
	v_mul_f32_e32 v0, 0xbfb8aa3b, v52
	v_exp_f32_e32 v0, v0
	s_nop 0
	v_add_f32_e32 v0, 1.0, v0
	v_rcp_f32_e32 v60, v0
	v_mul_f32_e32 v0, 0xbfb8aa3b, v53
	v_exp_f32_e32 v0, v0
	s_nop 0
	v_add_f32_e32 v0, 1.0, v0
	v_rcp_f32_e32 v61, v0
	s_nop 0
	v_pk_mul_f32 v[60:61], v[52:53], v[60:61]
	v_lshlrev_b32_e32 v52, 16, v55
	v_and_b32_e32 v53, 0xffff0000, v55
	v_pk_mul_f32 v[54:55], v[140:141], v[78:79] op_sel_hi:[0,1]
	v_pk_fma_f32 v[52:53], v[54:55], v[52:53], v[70:71]
	v_lshlrev_b32_e32 v54, 16, v59
	v_and_b32_e32 v55, 0xffff0000, v59
	v_pk_mul_f32 v[58:59], v[138:139], v[86:87] op_sel_hi:[0,1]
	v_pk_fma_f32 v[52:53], v[58:59], v[54:55], v[52:53]
	v_lshlrev_b32_e32 v54, 16, v63
	v_and_b32_e32 v55, 0xffff0000, v63
	v_pk_mul_f32 v[58:59], v[136:137], v[98:99] op_sel_hi:[0,1]
	v_pk_fma_f32 v[52:53], v[58:59], v[54:55], v[52:53]
	v_lshlrev_b32_e32 v54, 16, v67
	v_and_b32_e32 v55, 0xffff0000, v67
	v_pk_mul_f32 v[58:59], v[134:135], v[106:107] op_sel_hi:[0,1]
	v_pk_fma_f32 v[52:53], v[58:59], v[54:55], v[52:53]
	v_lshlrev_b32_e32 v106, 16, v36
	v_mul_f32_e32 v0, 0xbfb8aa3b, v52
	v_exp_f32_e32 v0, v0
	v_and_b32_e32 v107, 0xffff0000, v36
	v_lshlrev_b32_e32 v36, 16, v37
	v_and_b32_e32 v37, 0xffff0000, v37
	v_add_f32_e32 v0, 1.0, v0
	v_rcp_f32_e32 v54, v0
	v_mul_f32_e32 v0, 0xbfb8aa3b, v53
	v_exp_f32_e32 v0, v0
	s_nop 0
	v_add_f32_e32 v0, 1.0, v0
	v_rcp_f32_e32 v55, v0
	s_nop 0
	v_pk_mul_f32 v[58:59], v[52:53], v[54:55]
	v_cvt_pk_bf16_f32 v52, v72, v73
	v_cvt_pk_bf16_f32 v53, v56, v57
	v_cvt_pk_bf16_f32 v54, v60, v61
	v_cvt_pk_bf16_f32 v55, v58, v59
	global_store_dwordx4 v[152:153], v[52:55], off offset:1072
	ds_read_b128 v[56:59], v215 offset:6160
	s_nop 0
	ds_read_b128 v[52:55], v215 offset:6144
	ds_read_b128 v[60:63], v215 offset:16
	ds_read_b128 v[64:67], v215 offset:0
	ds_read_b128 v[68:71], v215 offset:1552
	ds_read_b128 v[72:75], v215 offset:1536
	ds_read_b128 v[76:79], v215 offset:3072
	s_nop 0
	ds_read_b128 v[80:83], v215 offset:3088
	s_nop 0
	ds_read_b128 v[84:87], v215 offset:4608
	s_nop 0
	ds_read_b128 v[88:91], v215 offset:4624
	s_waitcnt lgkmcnt(0)
; DI unsigned pk2h(float lo, float hi) { const f32x2h_t v = {lo, hi}; return __builtin_bit_cast(unsigned, __builtin_convertvector(v, bf16x2h_t)); }
; DI float silu_f(float x) { return x * __builtin_amdgcn_rcpf(1.f + __expf(-x)); }
; DI void ssd_local_unit(Frame& F, int l, int ch, int g) {
;     ...
;         for (int cc = 0; cc < 4; ++cc) {
;             const int lc = cg * 32 + cc * 8, c0 = part * 256 + g * 128 + lc;
;             float acc[8];
;             { const f32x4 b0 = *(const f32x4*)(cb + c0), b1 = *(const f32x4*)(cb + c0 + 4);
; #pragma unroll
;               for (int e = 0; e < 4; ++e) { acc[e] = b0[e]; acc[4 + e] = b1[e]; } }
; #pragma unroll
;             for (int j = 0; j < 4; ++j) { float x[8]; unpack8(raw[cc][j], x);
;                 const f32x4 w0 = *(const f32x4*)(cw + j * XC + c0), w1 = *(const f32x4*)(cw + j * XC + c0 + 4);
; #pragma unroll
;                 for (int e = 0; e < 4; ++e) { acc[e] += w0[e] * okm[j] * x[e]; acc[4 + e] += w1[e] * okm[j] * x[4 + e]; } }
; #pragma unroll
;             for (int e = 0; e < 8; ++e) acc[e] = silu_f(acc[e]);
;             v4u o; o.x = pk2h(acc[0], acc[1]); o.y = pk2h(acc[2], acc[3]); o.z = pk2h(acc[4], acc[5]); o.w = pk2h(acc[6], acc[7]);
;             *(v4u*)(xbcc + (size_t)(t0 + s) * XC + c0) = o;
;             if (part == 0) { const int r2 = lc >> 6; const float dtv = DT[r2 * 128 + s], sc = dtv * __expf(AC[r2 * 128 + 127] - AC[r2 * 128 + s]);
	v_pk_mul_f32 v[60:61], v[140:141], v[60:61] op_sel_hi:[0,1]
	s_nop 0
	v_pk_mul_f32 v[64:65], v[140:141], v[64:65] op_sel_hi:[0,1]
	v_pk_fma_f32 v[52:53], v[64:65], v[92:93], v[52:53]
	v_lshlrev_b32_e32 v64, 16, v120
	v_and_b32_e32 v65, 0xffff0000, v120
	s_nop 0
	v_pk_mul_f32 v[72:73], v[138:139], v[72:73] op_sel_hi:[0,1]
	v_pk_fma_f32 v[52:53], v[72:73], v[64:65], v[52:53]
	v_lshlrev_b32_e32 v64, 16, v124
	v_and_b32_e32 v65, 0xffff0000, v124
	s_nop 0
	v_pk_mul_f32 v[72:73], v[136:137], v[76:77] op_sel_hi:[0,1]
	v_pk_fma_f32 v[52:53], v[72:73], v[64:65], v[52:53]
	v_lshlrev_b32_e32 v64, 16, v128
	v_and_b32_e32 v65, 0xffff0000, v128
	s_nop 0
	v_pk_mul_f32 v[72:73], v[134:135], v[84:85] op_sel_hi:[0,1]
	v_pk_fma_f32 v[52:53], v[72:73], v[64:65], v[52:53]
	v_pk_mul_f32 v[66:67], v[140:141], v[66:67] op_sel_hi:[0,1]
	v_mul_f32_e32 v0, 0xbfb8aa3b, v52
	v_exp_f32_e32 v0, v0
	v_pk_mul_f32 v[62:63], v[140:141], v[62:63] op_sel_hi:[0,1]
	v_add_f32_e32 v0, 1.0, v0
	v_rcp_f32_e32 v64, v0
	v_mul_f32_e32 v0, 0xbfb8aa3b, v53
	v_exp_f32_e32 v0, v0
	s_nop 0
	v_add_f32_e32 v0, 1.0, v0
	v_rcp_f32_e32 v65, v0
	s_nop 0
	v_pk_mul_f32 v[52:53], v[52:53], v[64:65]
	v_lshlrev_b32_e32 v64, 16, v117
	v_and_b32_e32 v65, 0xffff0000, v117
	v_pk_fma_f32 v[54:55], v[66:67], v[64:65], v[54:55]
	v_lshlrev_b32_e32 v64, 16, v121
	v_and_b32_e32 v65, 0xffff0000, v121
	v_pk_mul_f32 v[66:67], v[138:139], v[74:75] op_sel_hi:[0,1]
	v_pk_fma_f32 v[54:55], v[66:67], v[64:65], v[54:55]
	v_lshlrev_b32_e32 v64, 16, v125
	v_and_b32_e32 v65, 0xffff0000, v125
	v_pk_mul_f32 v[66:67], v[136:137], v[78:79] op_sel_hi:[0,1]
	v_pk_fma_f32 v[54:55], v[66:67], v[64:65], v[54:55]
	v_lshlrev_b32_e32 v64, 16, v129
	v_and_b32_e32 v65, 0xffff0000, v129
	v_pk_mul_f32 v[66:67], v[134:135], v[86:87] op_sel_hi:[0,1]
	v_pk_fma_f32 v[54:55], v[66:67], v[64:65], v[54:55]
	s_nop 0
	v_mul_f32_e32 v0, 0xbfb8aa3b, v54
	v_exp_f32_e32 v0, v0
	s_nop 0
	v_add_f32_e32 v0, 1.0, v0
	v_rcp_f32_e32 v64, v0
	v_mul_f32_e32 v0, 0xbfb8aa3b, v55
	v_exp_f32_e32 v0, v0
	s_nop 0
	v_add_f32_e32 v0, 1.0, v0
	v_rcp_f32_e32 v65, v0
	s_nop 0
	v_pk_mul_f32 v[54:55], v[54:55], v[64:65]
	v_lshlrev_b32_e32 v64, 16, v118
	v_and_b32_e32 v65, 0xffff0000, v118
	v_pk_fma_f32 v[56:57], v[60:61], v[64:65], v[56:57]
	v_lshlrev_b32_e32 v60, 16, v122
	v_and_b32_e32 v61, 0xffff0000, v122
	v_pk_mul_f32 v[64:65], v[138:139], v[68:69] op_sel_hi:[0,1]
	v_pk_fma_f32 v[56:57], v[64:65], v[60:61], v[56:57]
	v_lshlrev_b32_e32 v60, 16, v126
	v_and_b32_e32 v61, 0xffff0000, v126
	v_pk_mul_f32 v[64:65], v[136:137], v[80:81] op_sel_hi:[0,1]
	v_pk_fma_f32 v[56:57], v[64:65], v[60:61], v[56:57]
	v_lshlrev_b32_e32 v60, 16, v130
	v_and_b32_e32 v61, 0xffff0000, v130
	s_nop 0
	v_pk_mul_f32 v[64:65], v[134:135], v[88:89] op_sel_hi:[0,1]
	v_pk_fma_f32 v[56:57], v[64:65], v[60:61], v[56:57]
	v_add_u32_e32 v64, s4, v164
	v_mul_f32_e32 v0, 0xbfb8aa3b, v56
	v_exp_f32_e32 v0, v0
	s_nop 0
	v_add_f32_e32 v0, 1.0, v0
	v_rcp_f32_e32 v60, v0
	v_mul_f32_e32 v0, 0xbfb8aa3b, v57
	v_exp_f32_e32 v0, v0
	s_nop 0
	v_add_f32_e32 v0, 1.0, v0
	v_rcp_f32_e32 v61, v0
	s_nop 0
	v_pk_mul_f32 v[56:57], v[56:57], v[60:61]
	v_lshlrev_b32_e32 v60, 16, v119
	v_and_b32_e32 v61, 0xffff0000, v119
	v_pk_fma_f32 v[58:59], v[62:63], v[60:61], v[58:59]
	v_lshlrev_b32_e32 v60, 16, v123
	v_and_b32_e32 v61, 0xffff0000, v123
	v_pk_mul_f32 v[62:63], v[138:139], v[70:71] op_sel_hi:[0,1]
	v_pk_fma_f32 v[58:59], v[62:63], v[60:61], v[58:59]
	v_lshlrev_b32_e32 v60, 16, v127
	v_and_b32_e32 v61, 0xffff0000, v127
	v_pk_mul_f32 v[62:63], v[136:137], v[82:83] op_sel_hi:[0,1]
	v_pk_fma_f32 v[58:59], v[62:63], v[60:61], v[58:59]
	v_lshlrev_b32_e32 v60, 16, v131
	v_and_b32_e32 v61, 0xffff0000, v131
	v_pk_mul_f32 v[62:63], v[134:135], v[90:91] op_sel_hi:[0,1]
	v_pk_fma_f32 v[58:59], v[62:63], v[60:61], v[58:59]
	v_cvt_pk_bf16_f32 v62, v56, v57
	v_mul_f32_e32 v0, 0xbfb8aa3b, v58
	v_exp_f32_e32 v0, v0
	s_nop 0
	v_add_f32_e32 v0, 1.0, v0
	v_rcp_f32_e32 v60, v0
	v_mul_f32_e32 v0, 0xbfb8aa3b, v59
	v_exp_f32_e32 v0, v0
	s_nop 0
	v_add_f32_e32 v0, 1.0, v0
	v_rcp_f32_e32 v61, v0
	v_and_b32_e32 v0, 0x80, v2
	v_add_lshl_u32 v0, v0, v1, 2
	v_add_u32_e32 v2, s41, v0
	v_pk_mul_f32 v[58:59], v[58:59], v[60:61]
	v_cvt_pk_bf16_f32 v60, v52, v53
	v_cvt_pk_bf16_f32 v61, v54, v55
	v_cvt_pk_bf16_f32 v63, v58, v59
	v_add_u32_e32 v0, s36, v0
	global_store_dwordx4 v[152:153], v[60:63], off
	ds_read_b32 v60, v2
	ds_read_b32 v0, v0
	v_lshl_or_b32 v2, v137, 8, v233
	v_add_u32_e32 v2, s36, v2
	ds_read_b32 v2, v2
	s_waitcnt lgkmcnt(0)
; __device__ __forceinline__ unsigned f2bf(float f) { unsigned u = __builtin_bit_cast(unsigned, f); return (u + 0x7fffu + ((u >> 16) & 1u)) >> 16; }
; DI unsigned pk2h(float lo, float hi) { const f32x2h_t v = {lo, hi}; return __builtin_bit_cast(unsigned, __builtin_convertvector(v, bf16x2h_t)); }
; DI float silu_f(float x) { return x * __builtin_amdgcn_rcpf(1.f + __expf(-x)); }
; DI void ssd_local_unit(Frame& F, int l, int ch, int g) {
;     ...
;         for (int cc = 0; cc < 4; ++cc) {
;             const int lc = cg * 32 + cc * 8, c0 = part * 256 + g * 128 + lc;
;             float acc[8];
;             { const f32x4 b0 = *(const f32x4*)(cb + c0), b1 = *(const f32x4*)(cb + c0 + 4);
; #pragma unroll
;               for (int e = 0; e < 4; ++e) { acc[e] = b0[e]; acc[4 + e] = b1[e]; } }
; #pragma unroll
;             for (int j = 0; j < 4; ++j) { float x[8]; unpack8(raw[cc][j], x);
;                 const f32x4 w0 = *(const f32x4*)(cw + j * XC + c0), w1 = *(const f32x4*)(cw + j * XC + c0 + 4);
; #pragma unroll
;                 for (int e = 0; e < 4; ++e) { acc[e] += w0[e] * okm[j] * x[e]; acc[4 + e] += w1[e] * okm[j] * x[4 + e]; } }
; #pragma unroll
;             for (int e = 0; e < 8; ++e) acc[e] = silu_f(acc[e]);
;             v4u o; o.x = pk2h(acc[0], acc[1]); o.y = pk2h(acc[2], acc[3]); o.z = pk2h(acc[4], acc[5]); o.w = pk2h(acc[6], acc[7]);
;             *(v4u*)(xbcc + (size_t)(t0 + s) * XC + c0) = o;
;             if (part == 0) { const int r2 = lc >> 6; const float dtv = DT[r2 * 128 + s], sc = dtv * __expf(AC[r2 * 128 + 127] - AC[r2 * 128 + s]);
; #pragma unroll
;                 for (int e = 0; e < 8; ++e) { XWT[(lc + e) * LP + s] = (bf16)f2bf(acc[e] * sc); XD[(lc + e) * LP + s] = (bf16)f2bf(acc[e] * dtv); } }
	v_sub_f32_e32 v0, v2, v0
	v_mul_f32_e32 v0, 0x3fb8aa3b, v0
	v_exp_f32_e32 v0, v0
	s_nop 0
	v_mul_f32_e32 v61, v60, v0
	v_mul_f32_e32 v0, v61, v52
	v_bfe_u32 v2, v0, 16, 1
	v_add3_u32 v0, v0, v2, s97
	v_mul_u32_u24_e32 v2, 0x1100, v137
	v_lshlrev_b32_e32 v2, 1, v2
	v_add_u32_e32 v62, v135, v2
	ds_write_b16_d16_hi v62, v0
	v_mul_f32_e32 v0, v60, v52
	v_bfe_u32 v52, v0, 16, 1
	v_add3_u32 v0, v0, v52, s97
	v_add_u32_e32 v63, v64, v2
	ds_write_b16_d16_hi v63, v0
	v_mul_f32_e32 v0, v61, v53
	v_bfe_u32 v2, v0, 16, 1
	v_add3_u32 v0, v0, v2, s97
	ds_write_b16_d16_hi v62, v0 offset:272
	v_mul_f32_e32 v0, v60, v53
	v_bfe_u32 v2, v0, 16, 1
	v_add3_u32 v0, v0, v2, s97
	ds_write_b16_d16_hi v63, v0 offset:272
	v_mul_f32_e32 v0, v61, v54
	v_bfe_u32 v2, v0, 16, 1
	v_add3_u32 v0, v0, v2, s97
	ds_write_b16_d16_hi v62, v0 offset:544
	v_mul_f32_e32 v0, v60, v54
	v_bfe_u32 v2, v0, 16, 1
	v_add3_u32 v0, v0, v2, s97
	ds_write_b16_d16_hi v63, v0 offset:544
	v_mul_f32_e32 v0, v61, v55
	v_bfe_u32 v2, v0, 16, 1
	v_add3_u32 v0, v0, v2, s97
	ds_write_b16_d16_hi v62, v0 offset:816
	v_mul_f32_e32 v0, v60, v55
	v_bfe_u32 v2, v0, 16, 1
	v_add3_u32 v0, v0, v2, s97
	ds_write_b16_d16_hi v63, v0 offset:816
	v_mul_f32_e32 v0, v61, v56
	v_bfe_u32 v2, v0, 16, 1
	v_add3_u32 v0, v0, v2, s97
	ds_write_b16_d16_hi v62, v0 offset:1088
	v_mul_f32_e32 v0, v60, v56
	v_bfe_u32 v2, v0, 16, 1
	v_add3_u32 v0, v0, v2, s97
	ds_write_b16_d16_hi v63, v0 offset:1088
	v_mul_f32_e32 v0, v61, v57
	v_bfe_u32 v2, v0, 16, 1
	v_add3_u32 v0, v0, v2, s97
	ds_write_b16_d16_hi v62, v0 offset:1360
	v_mul_f32_e32 v0, v60, v57
	v_bfe_u32 v2, v0, 16, 1
	v_add3_u32 v0, v0, v2, s97
	ds_write_b16_d16_hi v63, v0 offset:1360
	v_mul_f32_e32 v0, v61, v58
	v_bfe_u32 v2, v0, 16, 1
	v_add3_u32 v0, v0, v2, s97
	ds_write_b16_d16_hi v62, v0 offset:1632
	v_mul_f32_e32 v0, v60, v58
	v_bfe_u32 v2, v0, 16, 1
	v_add3_u32 v0, v0, v2, s97
	ds_write_b16_d16_hi v63, v0 offset:1632
	v_mul_f32_e32 v0, v61, v59
	v_bfe_u32 v2, v0, 16, 1
	v_add3_u32 v0, v0, v2, s97
	ds_write_b16_d16_hi v62, v0 offset:1904
	v_mul_f32_e32 v0, v60, v59
	v_bfe_u32 v2, v0, 16, 1
	v_add3_u32 v0, v0, v2, s97
	v_add_u32_e32 v2, s40, v141
	v_lshlrev_b64 v[52:53], 2, v[2:3]
	v_lshl_add_u64 v[58:59], s[2:3], 0, v[52:53]
	v_lshl_add_u64 v[52:53], s[0:1], 0, v[52:53]
	ds_write_b16_d16_hi v63, v0 offset:1904
	s_mov_b64 s[0:1], 0x1820
	v_add_co_u32_e32 v54, vcc, s64, v52
	ds_read_b128 v[66:69], v215 offset:6192
	ds_read_b128 v[70:73], v215 offset:6176
	ds_read_b128 v[74:77], v215 offset:48
	ds_read_b128 v[78:81], v215 offset:32
	ds_read_b128 v[82:85], v215 offset:1584
	ds_read_b128 v[86:89], v215 offset:1568
	v_lshl_add_u64 v[56:57], v[52:53], 0, s[0:1]
	v_addc_co_u32_e32 v55, vcc, 0, v53, vcc
	ds_read_b128 v[90:93], v215 offset:3104
	ds_read_b128 v[94:97], v215 offset:3120
	s_mov_b64 s[0:1], 0x2420
	v_add_co_u32_e32 v56, vcc, s42, v52
	v_lshl_add_u64 v[102:103], v[52:53], 0, s[0:1]
	s_nop 0
	v_addc_co_u32_e32 v57, vcc, 0, v53, vcc
	ds_read_b128 v[98:101], v215 offset:4640
	s_nop 0
	ds_read_b128 v[102:105], v215 offset:4656
	s_mov_b64 s[0:1], 0x1840
	s_or_b32 s2, s39, s18
	s_waitcnt lgkmcnt(0)
	v_pk_mul_f32 v[78:79], v[140:141], v[78:79] op_sel_hi:[0,1]
	v_pk_fma_f32 v[70:71], v[78:79], v[106:107], v[70:71]
	v_lshlrev_b32_e32 v78, 16, v40
	v_and_b32_e32 v79, 0xffff0000, v40
	s_nop 0
	v_pk_mul_f32 v[86:87], v[138:139], v[86:87] op_sel_hi:[0,1]
	v_pk_fma_f32 v[70:71], v[86:87], v[78:79], v[70:71]
	v_lshlrev_b32_e32 v78, 16, v44
	v_and_b32_e32 v79, 0xffff0000, v44
	s_nop 0
	v_pk_mul_f32 v[86:87], v[136:137], v[90:91] op_sel_hi:[0,1]
	v_pk_fma_f32 v[70:71], v[86:87], v[78:79], v[70:71]
	v_lshlrev_b32_e32 v78, 16, v48
	v_and_b32_e32 v79, 0xffff0000, v48
	s_nop 0
	v_pk_mul_f32 v[86:87], v[134:135], v[98:99] op_sel_hi:[0,1]
	v_pk_fma_f32 v[70:71], v[86:87], v[78:79], v[70:71]
	v_lshlrev_b32_e32 v40, 16, v41
	v_mul_f32_e32 v0, 0xbfb8aa3b, v70
	v_exp_f32_e32 v0, v0
	v_and_b32_e32 v41, 0xffff0000, v41
	v_add_f32_e32 v0, 1.0, v0
	v_rcp_f32_e32 v78, v0
	v_mul_f32_e32 v0, 0xbfb8aa3b, v71
	v_exp_f32_e32 v0, v0
	s_nop 0
	v_add_f32_e32 v0, 1.0, v0
	v_rcp_f32_e32 v79, v0
	s_nop 0
	v_pk_mul_f32 v[70:71], v[70:71], v[78:79]
	v_pk_mul_f32 v[78:79], v[140:141], v[80:81] op_sel_hi:[0,1]
	v_pk_fma_f32 v[36:37], v[78:79], v[36:37], v[72:73]
	v_pk_mul_f32 v[72:73], v[138:139], v[88:89] op_sel_hi:[0,1]
	v_pk_fma_f32 v[36:37], v[72:73], v[40:41], v[36:37]
	v_lshlrev_b32_e32 v40, 16, v45
	v_and_b32_e32 v41, 0xffff0000, v45
	v_pk_mul_f32 v[44:45], v[136:137], v[92:93] op_sel_hi:[0,1]
	v_pk_fma_f32 v[36:37], v[44:45], v[40:41], v[36:37]
	v_lshlrev_b32_e32 v40, 16, v49
	v_and_b32_e32 v41, 0xffff0000, v49
	v_pk_mul_f32 v[44:45], v[134:135], v[100:101] op_sel_hi:[0,1]
	v_pk_fma_f32 v[36:37], v[44:45], v[40:41], v[36:37]
	v_pk_mul_f32 v[48:49], v[138:139], v[82:83] op_sel_hi:[0,1]
	v_mul_f32_e32 v0, 0xbfb8aa3b, v36
	v_exp_f32_e32 v0, v0
	s_nop 0
	v_add_f32_e32 v0, 1.0, v0
	v_rcp_f32_e32 v40, v0
	v_mul_f32_e32 v0, 0xbfb8aa3b, v37
	v_exp_f32_e32 v0, v0
	s_nop 0
	v_add_f32_e32 v0, 1.0, v0
	v_rcp_f32_e32 v41, v0
	s_nop 0
	v_pk_mul_f32 v[44:45], v[36:37], v[40:41]
	v_lshlrev_b32_e32 v36, 16, v38
	v_and_b32_e32 v37, 0xffff0000, v38
	v_pk_mul_f32 v[40:41], v[140:141], v[74:75] op_sel_hi:[0,1]
	v_pk_fma_f32 v[36:37], v[40:41], v[36:37], v[66:67]
	v_lshlrev_b32_e32 v40, 16, v42
	v_and_b32_e32 v41, 0xffff0000, v42
	v_pk_fma_f32 v[36:37], v[48:49], v[40:41], v[36:37]
	v_lshlrev_b32_e32 v40, 16, v46
	v_and_b32_e32 v41, 0xffff0000, v46
	v_pk_mul_f32 v[48:49], v[136:137], v[94:95] op_sel_hi:[0,1]
	v_pk_fma_f32 v[36:37], v[48:49], v[40:41], v[36:37]
	v_lshlrev_b32_e32 v40, 16, v50
	v_and_b32_e32 v41, 0xffff0000, v50
; __device__ __forceinline__ unsigned f2bf(float f) { unsigned u = __builtin_bit_cast(unsigned, f); return (u + 0x7fffu + ((u >> 16) & 1u)) >> 16; }
; DI unsigned pk2h(float lo, float hi) { const f32x2h_t v = {lo, hi}; return __builtin_bit_cast(unsigned, __builtin_convertvector(v, bf16x2h_t)); }
; DI float silu_f(float x) { return x * __builtin_amdgcn_rcpf(1.f + __expf(-x)); }
; DI void ssd_local_unit(Frame& F, int l, int ch, int g) {
;     ...
;             for (int j = 0; j < 4; ++j) { float x[8]; unpack8(raw[cc][j], x);
;                 const f32x4 w0 = *(const f32x4*)(cw + j * XC + c0), w1 = *(const f32x4*)(cw + j * XC + c0 + 4);
; #pragma unroll
;                 for (int e = 0; e < 4; ++e) { acc[e] += w0[e] * okm[j] * x[e]; acc[4 + e] += w1[e] * okm[j] * x[4 + e]; } }
; #pragma unroll
;             for (int e = 0; e < 8; ++e) acc[e] = silu_f(acc[e]);
;             v4u o; o.x = pk2h(acc[0], acc[1]); o.y = pk2h(acc[2], acc[3]); o.z = pk2h(acc[4], acc[5]); o.w = pk2h(acc[6], acc[7]);
;             *(v4u*)(xbcc + (size_t)(t0 + s) * XC + c0) = o;
;             if (part == 0) { const int r2 = lc >> 6; const float dtv = DT[r2 * 128 + s], sc = dtv * __expf(AC[r2 * 128 + 127] - AC[r2 * 128 + s]);
; #pragma unroll
;                 for (int e = 0; e < 8; ++e) { XWT[(lc + e) * LP + s] = (bf16)f2bf(acc[e] * sc); XD[(lc + e) * LP + s] = (bf16)f2bf(acc[e] * dtv); } }
	s_nop 0
	v_pk_mul_f32 v[48:49], v[134:135], v[102:103] op_sel_hi:[0,1]
	v_pk_fma_f32 v[36:37], v[48:49], v[40:41], v[36:37]
	s_nop 0
	v_mul_f32_e32 v0, 0xbfb8aa3b, v36
	v_exp_f32_e32 v0, v0
	s_nop 0
	v_add_f32_e32 v0, 1.0, v0
	v_rcp_f32_e32 v40, v0
	v_mul_f32_e32 v0, 0xbfb8aa3b, v37
	v_exp_f32_e32 v0, v0
	s_nop 0
	v_add_f32_e32 v0, 1.0, v0
	v_rcp_f32_e32 v41, v0
	s_nop 0
	v_pk_mul_f32 v[48:49], v[36:37], v[40:41]
	v_lshlrev_b32_e32 v36, 16, v39
	v_and_b32_e32 v37, 0xffff0000, v39
	v_pk_mul_f32 v[38:39], v[140:141], v[76:77] op_sel_hi:[0,1]
	v_pk_fma_f32 v[36:37], v[38:39], v[36:37], v[68:69]
	v_lshlrev_b32_e32 v38, 16, v43
	v_and_b32_e32 v39, 0xffff0000, v43
	v_pk_mul_f32 v[40:41], v[138:139], v[84:85] op_sel_hi:[0,1]
	v_pk_fma_f32 v[36:37], v[40:41], v[38:39], v[36:37]
	v_lshlrev_b32_e32 v38, 16, v47
	v_and_b32_e32 v39, 0xffff0000, v47
	v_pk_mul_f32 v[40:41], v[136:137], v[96:97] op_sel_hi:[0,1]
	v_pk_fma_f32 v[36:37], v[40:41], v[38:39], v[36:37]
	v_lshlrev_b32_e32 v38, 16, v51
	v_and_b32_e32 v39, 0xffff0000, v51
	v_pk_mul_f32 v[40:41], v[134:135], v[104:105] op_sel_hi:[0,1]
	v_pk_fma_f32 v[36:37], v[40:41], v[38:39], v[36:37]
	v_lshl_add_u64 v[40:41], v[2:3], 1, v[142:143]
	v_mul_f32_e32 v0, 0xbfb8aa3b, v36
	v_exp_f32_e32 v0, v0
	v_lshl_add_u64 v[50:51], v[52:53], 0, s[0:1]
	s_mov_b64 s[0:1], 0x2440
	v_add_f32_e32 v0, 1.0, v0
	v_rcp_f32_e32 v38, v0
	v_mul_f32_e32 v0, 0xbfb8aa3b, v37
	v_exp_f32_e32 v0, v0
	s_nop 0
	v_add_f32_e32 v0, 1.0, v0
	v_rcp_f32_e32 v39, v0
	v_mul_f32_e32 v0, v61, v70
	v_bfe_u32 v2, v0, 16, 1
	v_add3_u32 v0, v0, v2, s97
	v_pk_mul_f32 v[42:43], v[36:37], v[38:39]
	v_mul_u32_u24_e32 v2, 0x88, v163
	v_cvt_pk_bf16_f32 v36, v70, v71
	v_cvt_pk_bf16_f32 v37, v44, v45
	v_cvt_pk_bf16_f32 v38, v48, v49
	v_cvt_pk_bf16_f32 v39, v42, v43
	v_lshlrev_b32_e32 v2, 1, v2
	global_store_dwordx4 v[40:41], v[36:39], off offset:16
	s_nop 1
	v_add_u32_e32 v36, v135, v2
	ds_write_b16_d16_hi v36, v0
	v_mul_f32_e32 v0, v60, v70
	v_bfe_u32 v36, v0, 16, 1
	v_add3_u32 v0, v0, v36, s97
	v_add_u32_e32 v2, v64, v2
	ds_write_b16_d16_hi v2, v0
	v_mul_f32_e32 v0, v61, v71
	v_bfe_u32 v2, v0, 16, 1
	v_add3_u32 v0, v0, v2, s97
	ds_write_b16_d16_hi v62, v0 offset:2448
	v_mul_f32_e32 v0, v60, v71
	v_bfe_u32 v2, v0, 16, 1
	v_add3_u32 v0, v0, v2, s97
	ds_write_b16_d16_hi v63, v0 offset:2448
	v_mul_f32_e32 v0, v61, v44
	v_bfe_u32 v2, v0, 16, 1
	v_add3_u32 v0, v0, v2, s97
	ds_write_b16_d16_hi v62, v0 offset:2720
	v_mul_f32_e32 v0, v60, v44
	v_bfe_u32 v2, v0, 16, 1
	v_add3_u32 v0, v0, v2, s97
	ds_write_b16_d16_hi v63, v0 offset:2720
	v_mul_f32_e32 v0, v61, v45
	v_bfe_u32 v2, v0, 16, 1
	v_add3_u32 v0, v0, v2, s97
	ds_write_b16_d16_hi v62, v0 offset:2992
	v_mul_f32_e32 v0, v60, v45
	v_bfe_u32 v2, v0, 16, 1
	v_add3_u32 v0, v0, v2, s97
	ds_write_b16_d16_hi v63, v0 offset:2992
	v_mul_f32_e32 v0, v61, v48
	v_bfe_u32 v2, v0, 16, 1
	v_add3_u32 v0, v0, v2, s97
	ds_write_b16_d16_hi v62, v0 offset:3264
	v_mul_f32_e32 v0, v60, v48
	v_bfe_u32 v2, v0, 16, 1
	v_add3_u32 v0, v0, v2, s97
	ds_write_b16_d16_hi v63, v0 offset:3264
	v_mul_f32_e32 v0, v61, v49
	v_bfe_u32 v2, v0, 16, 1
	v_add3_u32 v0, v0, v2, s97
	ds_write_b16_d16_hi v62, v0 offset:3536
	v_mul_f32_e32 v0, v60, v49
	v_bfe_u32 v2, v0, 16, 1
	v_add3_u32 v0, v0, v2, s97
	ds_write_b16_d16_hi v63, v0 offset:3536
	v_mul_f32_e32 v0, v61, v42
	v_bfe_u32 v2, v0, 16, 1
	v_add3_u32 v0, v0, v2, s97
	ds_write_b16_d16_hi v62, v0 offset:3808
	v_mul_f32_e32 v0, v60, v42
	v_bfe_u32 v2, v0, 16, 1
	v_add3_u32 v0, v0, v2, s97
	ds_write_b16_d16_hi v63, v0 offset:3808
	v_mul_f32_e32 v0, v61, v43
	v_bfe_u32 v2, v0, 16, 1
	v_add3_u32 v0, v0, v2, s97
	ds_write_b16_d16_hi v62, v0 offset:4080
	v_mul_f32_e32 v0, v60, v43
	v_bfe_u32 v2, v0, 16, 1
	v_add3_u32 v0, v0, v2, s97
	ds_write_b16_d16_hi v63, v0 offset:4080
	ds_read_b128 v[36:39], v215 offset:6224
	ds_read_b128 v[42:45], v215 offset:6208
	ds_read_b128 v[46:49], v215 offset:80
	ds_read_b128 v[66:69], v215 offset:64
	ds_read_b128 v[70:73], v215 offset:1616
	ds_read_b128 v[74:77], v215 offset:1600
	ds_read_b128 v[78:81], v215 offset:3136
	ds_read_b128 v[82:85], v215 offset:3152
	v_lshl_add_u64 v[50:51], v[52:53], 0, s[0:1]
	ds_read_b128 v[86:89], v215 offset:4672
	ds_read_b128 v[90:93], v215 offset:4688
	v_lshlrev_b32_e32 v50, 16, v20
	v_and_b32_e32 v51, 0xffff0000, v20
	v_lshlrev_b32_e32 v20, 16, v21
	v_and_b32_e32 v21, 0xffff0000, v21
	s_mov_b64 s[0:1], 0x1860
	s_waitcnt lgkmcnt(0)
; __device__ __forceinline__ unsigned f2bf(float f) { unsigned u = __builtin_bit_cast(unsigned, f); return (u + 0x7fffu + ((u >> 16) & 1u)) >> 16; }
; DI unsigned pk2h(float lo, float hi) { const f32x2h_t v = {lo, hi}; return __builtin_bit_cast(unsigned, __builtin_convertvector(v, bf16x2h_t)); }
; DI float silu_f(float x) { return x * __builtin_amdgcn_rcpf(1.f + __expf(-x)); }
; DI void ssd_local_unit(Frame& F, int l, int ch, int g) {
;     ...
;             for (int j = 0; j < 4; ++j) { float x[8]; unpack8(raw[cc][j], x);
;                 const f32x4 w0 = *(const f32x4*)(cw + j * XC + c0), w1 = *(const f32x4*)(cw + j * XC + c0 + 4);
; #pragma unroll
;                 for (int e = 0; e < 4; ++e) { acc[e] += w0[e] * okm[j] * x[e]; acc[4 + e] += w1[e] * okm[j] * x[4 + e]; } }
; #pragma unroll
;             for (int e = 0; e < 8; ++e) acc[e] = silu_f(acc[e]);
;             v4u o; o.x = pk2h(acc[0], acc[1]); o.y = pk2h(acc[2], acc[3]); o.z = pk2h(acc[4], acc[5]); o.w = pk2h(acc[6], acc[7]);
;             *(v4u*)(xbcc + (size_t)(t0 + s) * XC + c0) = o;
;             if (part == 0) { const int r2 = lc >> 6; const float dtv = DT[r2 * 128 + s], sc = dtv * __expf(AC[r2 * 128 + 127] - AC[r2 * 128 + s]);
; #pragma unroll
;                 for (int e = 0; e < 8; ++e) { XWT[(lc + e) * LP + s] = (bf16)f2bf(acc[e] * sc); XD[(lc + e) * LP + s] = (bf16)f2bf(acc[e] * dtv); } }
	v_pk_mul_f32 v[66:67], v[140:141], v[66:67] op_sel_hi:[0,1]
	v_pk_fma_f32 v[42:43], v[66:67], v[50:51], v[42:43]
	v_lshlrev_b32_e32 v50, 16, v24
	v_and_b32_e32 v51, 0xffff0000, v24
	s_nop 0
	v_pk_mul_f32 v[66:67], v[138:139], v[74:75] op_sel_hi:[0,1]
	v_pk_fma_f32 v[42:43], v[66:67], v[50:51], v[42:43]
	v_lshlrev_b32_e32 v50, 16, v28
	v_and_b32_e32 v51, 0xffff0000, v28
	s_nop 0
	v_pk_mul_f32 v[66:67], v[136:137], v[78:79] op_sel_hi:[0,1]
	v_pk_fma_f32 v[42:43], v[66:67], v[50:51], v[42:43]
	v_lshlrev_b32_e32 v50, 16, v32
	v_and_b32_e32 v51, 0xffff0000, v32
	s_nop 0
	v_pk_mul_f32 v[66:67], v[134:135], v[86:87] op_sel_hi:[0,1]
	v_pk_fma_f32 v[42:43], v[66:67], v[50:51], v[42:43]
	v_lshlrev_b32_e32 v24, 16, v25
	v_mul_f32_e32 v0, 0xbfb8aa3b, v42
	v_exp_f32_e32 v0, v0
	v_and_b32_e32 v25, 0xffff0000, v25
	v_add_f32_e32 v0, 1.0, v0
	v_rcp_f32_e32 v50, v0
	v_mul_f32_e32 v0, 0xbfb8aa3b, v43
	v_exp_f32_e32 v0, v0
	s_nop 0
	v_add_f32_e32 v0, 1.0, v0
	v_rcp_f32_e32 v51, v0
	s_nop 0
	v_pk_mul_f32 v[42:43], v[42:43], v[50:51]
	v_pk_mul_f32 v[50:51], v[140:141], v[68:69] op_sel_hi:[0,1]
	v_pk_fma_f32 v[20:21], v[50:51], v[20:21], v[44:45]
	v_pk_mul_f32 v[44:45], v[138:139], v[76:77] op_sel_hi:[0,1]
	v_pk_fma_f32 v[20:21], v[44:45], v[24:25], v[20:21]
	v_lshlrev_b32_e32 v24, 16, v29
	v_and_b32_e32 v25, 0xffff0000, v29
	v_pk_mul_f32 v[28:29], v[136:137], v[80:81] op_sel_hi:[0,1]
	v_pk_fma_f32 v[20:21], v[28:29], v[24:25], v[20:21]
	v_lshlrev_b32_e32 v24, 16, v33
	v_and_b32_e32 v25, 0xffff0000, v33
	v_pk_mul_f32 v[28:29], v[134:135], v[88:89] op_sel_hi:[0,1]
	v_pk_fma_f32 v[20:21], v[28:29], v[24:25], v[20:21]
	v_pk_mul_f32 v[28:29], v[140:141], v[46:47] op_sel_hi:[0,1]
	v_mul_f32_e32 v0, 0xbfb8aa3b, v20
	v_exp_f32_e32 v0, v0
	v_pk_mul_f32 v[32:33], v[138:139], v[70:71] op_sel_hi:[0,1]
	v_lshl_add_u64 v[50:51], v[52:53], 0, s[0:1]
	s_mov_b64 s[0:1], 0x2460
	v_add_f32_e32 v0, 1.0, v0
	v_rcp_f32_e32 v24, v0
	v_mul_f32_e32 v0, 0xbfb8aa3b, v21
	v_exp_f32_e32 v0, v0
	s_nop 0
	v_add_f32_e32 v0, 1.0, v0
	v_rcp_f32_e32 v25, v0
	s_nop 0
	v_pk_mul_f32 v[24:25], v[20:21], v[24:25]
	v_lshlrev_b32_e32 v20, 16, v22
	v_and_b32_e32 v21, 0xffff0000, v22
	v_pk_fma_f32 v[20:21], v[28:29], v[20:21], v[36:37]
	v_lshlrev_b32_e32 v28, 16, v26
	v_and_b32_e32 v29, 0xffff0000, v26
	v_pk_fma_f32 v[20:21], v[32:33], v[28:29], v[20:21]
	v_lshlrev_b32_e32 v28, 16, v30
	v_and_b32_e32 v29, 0xffff0000, v30
	v_pk_mul_f32 v[32:33], v[136:137], v[82:83] op_sel_hi:[0,1]
	v_pk_fma_f32 v[20:21], v[32:33], v[28:29], v[20:21]
	v_lshlrev_b32_e32 v28, 16, v34
	v_and_b32_e32 v29, 0xffff0000, v34
	s_nop 0
	v_pk_mul_f32 v[32:33], v[134:135], v[90:91] op_sel_hi:[0,1]
	v_pk_fma_f32 v[20:21], v[32:33], v[28:29], v[20:21]
	s_nop 0
	v_mul_f32_e32 v0, 0xbfb8aa3b, v20
	v_exp_f32_e32 v0, v0
	s_nop 0
	v_add_f32_e32 v0, 1.0, v0
	v_rcp_f32_e32 v28, v0
	v_mul_f32_e32 v0, 0xbfb8aa3b, v21
	v_exp_f32_e32 v0, v0
	s_nop 0
	v_add_f32_e32 v0, 1.0, v0
	v_rcp_f32_e32 v29, v0
	s_nop 0
	v_pk_mul_f32 v[28:29], v[20:21], v[28:29]
	v_lshlrev_b32_e32 v20, 16, v23
	v_and_b32_e32 v21, 0xffff0000, v23
	v_pk_mul_f32 v[22:23], v[140:141], v[48:49] op_sel_hi:[0,1]
	v_pk_fma_f32 v[20:21], v[22:23], v[20:21], v[38:39]
	v_lshlrev_b32_e32 v22, 16, v27
	v_and_b32_e32 v23, 0xffff0000, v27
	v_pk_mul_f32 v[26:27], v[138:139], v[72:73] op_sel_hi:[0,1]
	v_pk_fma_f32 v[20:21], v[26:27], v[22:23], v[20:21]
	v_lshlrev_b32_e32 v22, 16, v31
	v_and_b32_e32 v23, 0xffff0000, v31
	v_pk_mul_f32 v[26:27], v[136:137], v[84:85] op_sel_hi:[0,1]
	v_pk_fma_f32 v[20:21], v[26:27], v[22:23], v[20:21]
	v_lshlrev_b32_e32 v22, 16, v35
	v_and_b32_e32 v23, 0xffff0000, v35
	v_pk_mul_f32 v[26:27], v[134:135], v[92:93] op_sel_hi:[0,1]
	v_pk_fma_f32 v[20:21], v[26:27], v[22:23], v[20:21]
	s_nop 0
	v_mul_f32_e32 v0, 0xbfb8aa3b, v20
	v_exp_f32_e32 v0, v0
	s_nop 0
	v_add_f32_e32 v0, 1.0, v0
	v_rcp_f32_e32 v22, v0
	v_mul_f32_e32 v0, 0xbfb8aa3b, v21
	v_exp_f32_e32 v0, v0
	s_nop 0
	v_add_f32_e32 v0, 1.0, v0
	v_rcp_f32_e32 v23, v0
	v_mul_f32_e32 v0, v61, v42
	v_bfe_u32 v2, v0, 16, 1
	v_add3_u32 v0, v0, v2, s97
	v_pk_mul_f32 v[26:27], v[20:21], v[22:23]
	v_mul_u32_u24_e32 v2, 0x88, v162
	v_cvt_pk_bf16_f32 v20, v42, v43
	v_cvt_pk_bf16_f32 v21, v24, v25
	v_cvt_pk_bf16_f32 v22, v28, v29
	v_cvt_pk_bf16_f32 v23, v26, v27
	v_lshlrev_b32_e32 v2, 1, v2
	global_store_dwordx4 v[40:41], v[20:23], off offset:32
	s_nop 1
	v_add_u32_e32 v20, v135, v2
	ds_write_b16_d16_hi v20, v0
	v_mul_f32_e32 v0, v60, v42
	v_bfe_u32 v20, v0, 16, 1
	v_add3_u32 v0, v0, v20, s97
	v_add_u32_e32 v2, v64, v2
	ds_write_b16_d16_hi v2, v0
	v_mul_f32_e32 v0, v61, v43
	v_bfe_u32 v2, v0, 16, 1
	v_add3_u32 v0, v0, v2, s97
	ds_write_b16_d16_hi v62, v0 offset:4624
	v_mul_f32_e32 v0, v60, v43
	v_bfe_u32 v2, v0, 16, 1
	v_add3_u32 v0, v0, v2, s97
	ds_write_b16_d16_hi v63, v0 offset:4624
	v_mul_f32_e32 v0, v61, v24
	v_bfe_u32 v2, v0, 16, 1
	v_add3_u32 v0, v0, v2, s97
	ds_write_b16_d16_hi v62, v0 offset:4896
	v_mul_f32_e32 v0, v60, v24
	v_bfe_u32 v2, v0, 16, 1
	v_add3_u32 v0, v0, v2, s97
	ds_write_b16_d16_hi v63, v0 offset:4896
	v_mul_f32_e32 v0, v61, v25
	v_bfe_u32 v2, v0, 16, 1
	v_add3_u32 v0, v0, v2, s97
	ds_write_b16_d16_hi v62, v0 offset:5168
	v_mul_f32_e32 v0, v60, v25
	v_bfe_u32 v2, v0, 16, 1
	v_add3_u32 v0, v0, v2, s97
	ds_write_b16_d16_hi v63, v0 offset:5168
	v_mul_f32_e32 v0, v61, v28
	v_bfe_u32 v2, v0, 16, 1
	v_add3_u32 v0, v0, v2, s97
	ds_write_b16_d16_hi v62, v0 offset:5440
	v_mul_f32_e32 v0, v60, v28
	v_bfe_u32 v2, v0, 16, 1
	v_add3_u32 v0, v0, v2, s97
	ds_write_b16_d16_hi v63, v0 offset:5440
	v_mul_f32_e32 v0, v61, v29
	v_bfe_u32 v2, v0, 16, 1
	v_add3_u32 v0, v0, v2, s97
	ds_write_b16_d16_hi v62, v0 offset:5712
	v_mul_f32_e32 v0, v60, v29
	v_bfe_u32 v2, v0, 16, 1
	v_add3_u32 v0, v0, v2, s97
	ds_write_b16_d16_hi v63, v0 offset:5712
	v_mul_f32_e32 v0, v61, v26
	v_bfe_u32 v2, v0, 16, 1
	v_add3_u32 v0, v0, v2, s97
	ds_write_b16_d16_hi v62, v0 offset:5984
	v_mul_f32_e32 v0, v60, v26
	v_bfe_u32 v2, v0, 16, 1
	v_add3_u32 v0, v0, v2, s97
	ds_write_b16_d16_hi v63, v0 offset:5984
	v_mul_f32_e32 v0, v61, v27
	v_bfe_u32 v2, v0, 16, 1
	v_add3_u32 v0, v0, v2, s97
	ds_write_b16_d16_hi v62, v0 offset:6256
	v_mul_f32_e32 v0, v60, v27
	v_bfe_u32 v2, v0, 16, 1
	v_add3_u32 v0, v0, v2, s97
	ds_write_b16_d16_hi v63, v0 offset:6256
	ds_read_b128 v[20:23], v215 offset:6256
	ds_read_b128 v[24:27], v215 offset:6240
	ds_read_b128 v[28:31], v215 offset:112
	ds_read_b128 v[32:35], v215 offset:96
	ds_read_b128 v[36:39], v215 offset:1648
	ds_read_b128 v[42:45], v215 offset:1632
	ds_read_b128 v[46:49], v215 offset:3168
	ds_read_b128 v[66:69], v215 offset:3184
	v_lshl_add_u64 v[54:55], v[52:53], 0, s[0:1]
	ds_read_b128 v[50:53], v215 offset:4704
	s_nop 0
	ds_read_b128 v[54:57], v215 offset:4720
	v_lshlrev_b32_e32 v58, 16, v4
	v_and_b32_e32 v59, 0xffff0000, v4
	v_lshlrev_b32_e32 v4, 16, v5
	v_and_b32_e32 v5, 0xffff0000, v5
	s_waitcnt lgkmcnt(0)
; __device__ __forceinline__ unsigned f2bf(float f) { unsigned u = __builtin_bit_cast(unsigned, f); return (u + 0x7fffu + ((u >> 16) & 1u)) >> 16; }
; DI unsigned pk2h(float lo, float hi) { const f32x2h_t v = {lo, hi}; return __builtin_bit_cast(unsigned, __builtin_convertvector(v, bf16x2h_t)); }
; DI float silu_f(float x) { return x * __builtin_amdgcn_rcpf(1.f + __expf(-x)); }
; DI void ssd_local_unit(Frame& F, int l, int ch, int g) {
;     ...
;             for (int j = 0; j < 4; ++j) { float x[8]; unpack8(raw[cc][j], x);
;                 const f32x4 w0 = *(const f32x4*)(cw + j * XC + c0), w1 = *(const f32x4*)(cw + j * XC + c0 + 4);
; #pragma unroll
;                 for (int e = 0; e < 4; ++e) { acc[e] += w0[e] * okm[j] * x[e]; acc[4 + e] += w1[e] * okm[j] * x[4 + e]; } }
; #pragma unroll
;             for (int e = 0; e < 8; ++e) acc[e] = silu_f(acc[e]);
;             v4u o; o.x = pk2h(acc[0], acc[1]); o.y = pk2h(acc[2], acc[3]); o.z = pk2h(acc[4], acc[5]); o.w = pk2h(acc[6], acc[7]);
;             *(v4u*)(xbcc + (size_t)(t0 + s) * XC + c0) = o;
;             if (part == 0) { const int r2 = lc >> 6; const float dtv = DT[r2 * 128 + s], sc = dtv * __expf(AC[r2 * 128 + 127] - AC[r2 * 128 + s]);
; #pragma unroll
;                 for (int e = 0; e < 8; ++e) { XWT[(lc + e) * LP + s] = (bf16)f2bf(acc[e] * sc); XD[(lc + e) * LP + s] = (bf16)f2bf(acc[e] * dtv); } }
;     ...
;     __syncthreads();
;     const int w = F.wave, r = F.lane & 15, q = F.lane >> 4;
	v_pk_mul_f32 v[32:33], v[140:141], v[32:33] op_sel_hi:[0,1]
	v_pk_fma_f32 v[24:25], v[32:33], v[58:59], v[24:25]
	v_lshlrev_b32_e32 v32, 16, v8
	v_and_b32_e32 v33, 0xffff0000, v8
	s_nop 0
	v_pk_mul_f32 v[42:43], v[138:139], v[42:43] op_sel_hi:[0,1]
	v_pk_fma_f32 v[24:25], v[42:43], v[32:33], v[24:25]
	v_lshlrev_b32_e32 v32, 16, v12
	v_and_b32_e32 v33, 0xffff0000, v12
	s_nop 0
	v_pk_mul_f32 v[42:43], v[136:137], v[46:47] op_sel_hi:[0,1]
	v_pk_fma_f32 v[24:25], v[42:43], v[32:33], v[24:25]
	v_lshlrev_b32_e32 v32, 16, v16
	v_and_b32_e32 v33, 0xffff0000, v16
	s_nop 0
	v_pk_mul_f32 v[42:43], v[134:135], v[50:51] op_sel_hi:[0,1]
	v_pk_fma_f32 v[24:25], v[42:43], v[32:33], v[24:25]
	v_lshlrev_b32_e32 v8, 16, v9
	v_mul_f32_e32 v0, 0xbfb8aa3b, v24
	v_exp_f32_e32 v0, v0
	v_and_b32_e32 v9, 0xffff0000, v9
	v_add_f32_e32 v0, 1.0, v0
	v_rcp_f32_e32 v32, v0
	v_mul_f32_e32 v0, 0xbfb8aa3b, v25
	v_exp_f32_e32 v0, v0
	s_nop 0
	v_add_f32_e32 v0, 1.0, v0
	v_rcp_f32_e32 v33, v0
	s_nop 0
	v_pk_mul_f32 v[24:25], v[24:25], v[32:33]
	v_pk_mul_f32 v[32:33], v[140:141], v[34:35] op_sel_hi:[0,1]
	v_pk_fma_f32 v[4:5], v[32:33], v[4:5], v[26:27]
	v_pk_mul_f32 v[26:27], v[138:139], v[44:45] op_sel_hi:[0,1]
	v_pk_fma_f32 v[4:5], v[26:27], v[8:9], v[4:5]
	v_lshlrev_b32_e32 v8, 16, v13
	v_and_b32_e32 v9, 0xffff0000, v13
	v_pk_mul_f32 v[12:13], v[136:137], v[48:49] op_sel_hi:[0,1]
	v_pk_fma_f32 v[4:5], v[12:13], v[8:9], v[4:5]
	v_lshlrev_b32_e32 v8, 16, v17
	v_and_b32_e32 v9, 0xffff0000, v17
	v_pk_mul_f32 v[12:13], v[134:135], v[52:53] op_sel_hi:[0,1]
	v_pk_fma_f32 v[4:5], v[12:13], v[8:9], v[4:5]
	v_pk_mul_f32 v[12:13], v[140:141], v[28:29] op_sel_hi:[0,1]
	v_mul_f32_e32 v0, 0xbfb8aa3b, v4
	v_exp_f32_e32 v0, v0
	v_pk_mul_f32 v[16:17], v[138:139], v[36:37] op_sel_hi:[0,1]
	v_add_f32_e32 v0, 1.0, v0
	v_rcp_f32_e32 v8, v0
	v_mul_f32_e32 v0, 0xbfb8aa3b, v5
	v_exp_f32_e32 v0, v0
	s_nop 0
	v_add_f32_e32 v0, 1.0, v0
	v_rcp_f32_e32 v9, v0
	s_nop 0
	v_pk_mul_f32 v[8:9], v[4:5], v[8:9]
	v_lshlrev_b32_e32 v4, 16, v6
	v_and_b32_e32 v5, 0xffff0000, v6
	v_pk_fma_f32 v[4:5], v[12:13], v[4:5], v[20:21]
	v_lshlrev_b32_e32 v12, 16, v10
	v_and_b32_e32 v13, 0xffff0000, v10
	v_pk_fma_f32 v[4:5], v[16:17], v[12:13], v[4:5]
	v_lshlrev_b32_e32 v12, 16, v14
	v_and_b32_e32 v13, 0xffff0000, v14
	v_pk_mul_f32 v[16:17], v[136:137], v[66:67] op_sel_hi:[0,1]
	v_pk_fma_f32 v[4:5], v[16:17], v[12:13], v[4:5]
	v_lshlrev_b32_e32 v12, 16, v18
	v_and_b32_e32 v13, 0xffff0000, v18
	s_nop 0
	v_pk_mul_f32 v[16:17], v[134:135], v[54:55] op_sel_hi:[0,1]
	v_pk_fma_f32 v[4:5], v[16:17], v[12:13], v[4:5]
	s_nop 0
	v_mul_f32_e32 v0, 0xbfb8aa3b, v4
	v_exp_f32_e32 v0, v0
	s_nop 0
	v_add_f32_e32 v0, 1.0, v0
	v_rcp_f32_e32 v12, v0
	v_mul_f32_e32 v0, 0xbfb8aa3b, v5
	v_exp_f32_e32 v0, v0
	s_nop 0
	v_add_f32_e32 v0, 1.0, v0
	v_rcp_f32_e32 v13, v0
	s_nop 0
	v_pk_mul_f32 v[12:13], v[4:5], v[12:13]
	v_lshlrev_b32_e32 v4, 16, v7
	v_and_b32_e32 v5, 0xffff0000, v7
	v_pk_mul_f32 v[6:7], v[140:141], v[30:31] op_sel_hi:[0,1]
	v_pk_fma_f32 v[4:5], v[6:7], v[4:5], v[22:23]
	v_lshlrev_b32_e32 v6, 16, v11
	v_and_b32_e32 v7, 0xffff0000, v11
	v_pk_mul_f32 v[10:11], v[138:139], v[38:39] op_sel_hi:[0,1]
	v_pk_fma_f32 v[4:5], v[10:11], v[6:7], v[4:5]
	v_lshlrev_b32_e32 v6, 16, v15
	v_and_b32_e32 v7, 0xffff0000, v15
	v_pk_mul_f32 v[10:11], v[136:137], v[68:69] op_sel_hi:[0,1]
	v_pk_fma_f32 v[4:5], v[10:11], v[6:7], v[4:5]
	v_lshlrev_b32_e32 v6, 16, v19
	v_and_b32_e32 v7, 0xffff0000, v19
	v_pk_mul_f32 v[10:11], v[134:135], v[56:57] op_sel_hi:[0,1]
	v_pk_fma_f32 v[4:5], v[10:11], v[6:7], v[4:5]
	s_nop 0
	v_mul_f32_e32 v0, 0xbfb8aa3b, v4
	v_exp_f32_e32 v0, v0
	s_nop 0
	v_add_f32_e32 v0, 1.0, v0
	v_rcp_f32_e32 v6, v0
	v_mul_f32_e32 v0, 0xbfb8aa3b, v5
	v_exp_f32_e32 v0, v0
	s_nop 0
	v_add_f32_e32 v0, 1.0, v0
	v_rcp_f32_e32 v7, v0
	v_mul_f32_e32 v0, v61, v24
	v_bfe_u32 v2, v0, 16, 1
	v_add3_u32 v0, v0, v2, s97
	v_pk_mul_f32 v[10:11], v[4:5], v[6:7]
	v_mul_u32_u24_e32 v2, 0x88, v139
	v_cvt_pk_bf16_f32 v4, v24, v25
	v_cvt_pk_bf16_f32 v5, v8, v9
	v_cvt_pk_bf16_f32 v6, v12, v13
	v_cvt_pk_bf16_f32 v7, v10, v11
	v_lshlrev_b32_e32 v2, 1, v2
	global_store_dwordx4 v[40:41], v[4:7], off offset:48
	s_nop 1
	v_add_u32_e32 v4, v135, v2
	ds_write_b16_d16_hi v4, v0
	v_mul_f32_e32 v0, v60, v24
	v_bfe_u32 v4, v0, 16, 1
	v_add3_u32 v0, v0, v4, s97
	v_add_u32_e32 v2, v64, v2
	ds_write_b16_d16_hi v2, v0
	v_mul_f32_e32 v0, v61, v25
	v_bfe_u32 v2, v0, 16, 1
	v_add3_u32 v0, v0, v2, s97
	ds_write_b16_d16_hi v62, v0 offset:6800
	v_mul_f32_e32 v0, v60, v25
	v_bfe_u32 v2, v0, 16, 1
	v_add3_u32 v0, v0, v2, s97
	ds_write_b16_d16_hi v63, v0 offset:6800
	v_mul_f32_e32 v0, v61, v8
	v_bfe_u32 v2, v0, 16, 1
	v_add3_u32 v0, v0, v2, s97
	ds_write_b16_d16_hi v62, v0 offset:7072
	v_mul_f32_e32 v0, v60, v8
	v_bfe_u32 v2, v0, 16, 1
	v_add3_u32 v0, v0, v2, s97
	ds_write_b16_d16_hi v63, v0 offset:7072
	v_mul_f32_e32 v0, v61, v9
	v_bfe_u32 v2, v0, 16, 1
	v_add3_u32 v0, v0, v2, s97
	ds_write_b16_d16_hi v62, v0 offset:7344
	v_mul_f32_e32 v0, v60, v9
	v_bfe_u32 v2, v0, 16, 1
	v_add3_u32 v0, v0, v2, s97
	ds_write_b16_d16_hi v63, v0 offset:7344
	v_mul_f32_e32 v0, v61, v12
	v_bfe_u32 v2, v0, 16, 1
	v_add3_u32 v0, v0, v2, s97
	ds_write_b16_d16_hi v62, v0 offset:7616
	v_mul_f32_e32 v0, v60, v12
	v_bfe_u32 v2, v0, 16, 1
	v_add3_u32 v0, v0, v2, s97
	ds_write_b16_d16_hi v63, v0 offset:7616
	v_mul_f32_e32 v0, v61, v13
	v_bfe_u32 v2, v0, 16, 1
	v_add3_u32 v0, v0, v2, s97
	ds_write_b16_d16_hi v62, v0 offset:7888
	v_mul_f32_e32 v0, v60, v13
	v_bfe_u32 v2, v0, 16, 1
	v_add3_u32 v0, v0, v2, s97
	ds_write_b16_d16_hi v63, v0 offset:7888
	v_mul_f32_e32 v0, v61, v10
	v_bfe_u32 v2, v0, 16, 1
	v_add3_u32 v0, v0, v2, s97
	ds_write_b16_d16_hi v62, v0 offset:8160
	v_mul_f32_e32 v0, v60, v10
	v_bfe_u32 v2, v0, 16, 1
	v_add3_u32 v0, v0, v2, s97
	ds_write_b16_d16_hi v63, v0 offset:8160
	v_mul_f32_e32 v0, v61, v11
	v_bfe_u32 v2, v0, 16, 1
	v_add3_u32 v0, v0, v2, s97
	ds_write_b16_d16_hi v62, v0 offset:8432
	v_mul_f32_e32 v0, v60, v11
	v_bfe_u32 v2, v0, 16, 1
	v_add3_u32 v0, v0, v2, s97
	ds_write_b16_d16_hi v63, v0 offset:8432
	v_and_b32_e32 v2, 15, v132
	v_and_b32_e32 v0, 48, v133
	v_lshl_or_b32 v4, s37, 4, v2
	v_add_u32_e32 v0, s19, v0
	v_mad_u64_u32 v[48:49], s[0:1], v4, s66, v[0:1]
	v_mad_u32_u24 v0, v2, s66, v0
	s_waitcnt lgkmcnt(0)
	s_barrier
; #define LAS __attribute__((address_space(3)))
; DI f32x4 mfma16(bf16x8 a, bf16x8 b, f32x4 c) { asm volatile("s_nop 3" : "+v"(a), "+v"(b)); return __builtin_amdgcn_mfma_f32_16x16x32_bf16(a, b, c, 0, 0, 0); }
; DI void ssd_local_unit(Frame& F, int l, int ch, int g) {
;     ...
;     const int w = F.wave, r = F.lane & 15, q = F.lane >> 4;
;     f32x4 acc[8];
; #pragma unroll
;     for (int nt = 0; nt < 8; ++nt) acc[nt] = (f32x4){0.f, 0.f, 0.f, 0.f};
; #pragma unroll
;     for (int ks = 0; ks < 4; ++ks) { const bf16x8 a = *(const LAS bf16x8*)(XWT + (16 * w + r) * LP + 32 * ks + 8 * q);
; #pragma unroll
;         for (int nt = 0; nt < 8; ++nt) { const bf16x8 b = *(const LAS bf16x8*)(BT + (16 * nt + r) * LP + 32 * ks + 8 * q); acc[nt] = mfma16(a, b, acc[nt]); } }
	ds_read_b128 v[4:7], v0 offset:34816
	ds_read_b128 v[8:11], v48
	s_ashr_i32 s0, s38, 8
	s_add_i32 s0, s0, s2
	s_ashr_i32 s1, s0, 31
	s_lshl_b64 s[0:1], s[0:1], 15
	s_waitcnt lgkmcnt(0)
	v_mov_b64_e32 v[14:15], v[10:11]
	v_mov_b64_e32 v[12:13], v[8:9]
	s_nop 3
	v_mov_b64_e32 v[18:19], v[10:11]
	v_mov_b64_e32 v[16:17], v[8:9]
	v_mfma_f32_16x16x32_bf16 v[4:7], v[4:7], v[12:15], 0
	ds_read_b128 v[12:15], v0 offset:39168
	s_waitcnt lgkmcnt(0)
	s_nop 3
	v_mov_b64_e32 v[22:23], v[10:11]
	v_mfma_f32_16x16x32_bf16 v[12:15], v[12:15], v[16:19], 0
	ds_read_b128 v[16:19], v0 offset:43520
	v_mov_b64_e32 v[20:21], v[8:9]
	s_waitcnt lgkmcnt(0)
	s_nop 3
	v_mov_b64_e32 v[26:27], v[10:11]
	v_mov_b64_e32 v[24:25], v[8:9]
	v_mfma_f32_16x16x32_bf16 v[16:19], v[16:19], v[20:23], 0
	ds_read_b128 v[20:23], v0 offset:47872
	s_waitcnt lgkmcnt(0)
	s_nop 3
	v_mov_b64_e32 v[30:31], v[10:11]
	v_mfma_f32_16x16x32_bf16 v[20:23], v[20:23], v[24:27], 0
	ds_read_b128 v[24:27], v0 offset:52224
	v_mov_b64_e32 v[28:29], v[8:9]
	s_waitcnt lgkmcnt(0)
	s_nop 3
	v_mov_b64_e32 v[34:35], v[10:11]
	v_mov_b64_e32 v[32:33], v[8:9]
	v_mfma_f32_16x16x32_bf16 v[24:27], v[24:27], v[28:31], 0
	ds_read_b128 v[28:31], v0 offset:56576
	s_waitcnt lgkmcnt(0)
	s_nop 3
	v_mov_b64_e32 v[38:39], v[10:11]
	v_mfma_f32_16x16x32_bf16 v[28:31], v[28:31], v[32:35], 0
	ds_read_b128 v[32:35], v0 offset:60928
	v_mov_b64_e32 v[36:37], v[8:9]
	s_waitcnt lgkmcnt(0)
	s_nop 3
	s_add_u32 s0, s20, s0
	s_addc_u32 s1, s21, s1
	v_mfma_f32_16x16x32_bf16 v[32:35], v[32:35], v[36:39], 0
	ds_read_b128 v[36:39], v0 offset:65280
	s_waitcnt lgkmcnt(0)
	s_nop 3
	v_lshlrev_b32_e32 v2, 2, v2
	v_mfma_f32_16x16x32_bf16 v[8:11], v[36:39], v[8:11], 0
	ds_read_b128 v[36:39], v0 offset:34880
	ds_read_b128 v[40:43], v48 offset:64
	s_waitcnt lgkmcnt(0)
	v_mov_b64_e32 v[46:47], v[42:43]
	v_mov_b64_e32 v[44:45], v[40:41]
	s_nop 3
	s_nop 1
	v_mfma_f32_16x16x32_bf16 v[4:7], v[36:39], v[44:47], v[4:7]
	v_mov_b64_e32 v[46:47], v[42:43]
	ds_read_b128 v[36:39], v0 offset:39232
	v_mov_b64_e32 v[44:45], v[40:41]
	s_waitcnt lgkmcnt(0)
	s_nop 3
	s_nop 0
	v_mfma_f32_16x16x32_bf16 v[12:15], v[36:39], v[44:47], v[12:15]
	v_mov_b64_e32 v[46:47], v[42:43]
	ds_read_b128 v[36:39], v0 offset:43584
	v_mov_b64_e32 v[44:45], v[40:41]
	s_waitcnt lgkmcnt(0)
	s_nop 3
	s_nop 0
	v_mfma_f32_16x16x32_bf16 v[16:19], v[36:39], v[44:47], v[16:19]
	v_mov_b64_e32 v[46:47], v[42:43]
	ds_read_b128 v[36:39], v0 offset:47936
	v_mov_b64_e32 v[44:45], v[40:41]
	s_waitcnt lgkmcnt(0)
	s_nop 3
	s_nop 0
	v_mfma_f32_16x16x32_bf16 v[20:23], v[36:39], v[44:47], v[20:23]
	v_mov_b64_e32 v[46:47], v[42:43]
	ds_read_b128 v[36:39], v0 offset:52288
	v_mov_b64_e32 v[44:45], v[40:41]
	s_waitcnt lgkmcnt(0)
	s_nop 3
	s_nop 0
	v_mfma_f32_16x16x32_bf16 v[24:27], v[36:39], v[44:47], v[24:27]
	v_mov_b64_e32 v[46:47], v[42:43]
	ds_read_b128 v[36:39], v0 offset:56640
	v_mov_b64_e32 v[44:45], v[40:41]
	s_waitcnt lgkmcnt(0)
	s_nop 3
	s_nop 0
	v_mfma_f32_16x16x32_bf16 v[28:31], v[36:39], v[44:47], v[28:31]
	v_mov_b64_e32 v[46:47], v[42:43]
	ds_read_b128 v[36:39], v0 offset:60992
	v_mov_b64_e32 v[44:45], v[40:41]
	s_waitcnt lgkmcnt(0)
	s_nop 3
	s_nop 0
	v_mfma_f32_16x16x32_bf16 v[32:35], v[36:39], v[44:47], v[32:35]
	ds_read_b128 v[36:39], v0 offset:65344
	s_waitcnt lgkmcnt(0)
	s_nop 3
	s_nop 0
	v_mfma_f32_16x16x32_bf16 v[8:11], v[36:39], v[40:43], v[8:11]
	ds_read_b128 v[36:39], v0 offset:34944
	ds_read_b128 v[40:43], v48 offset:128
	s_waitcnt lgkmcnt(0)
	v_mov_b64_e32 v[46:47], v[42:43]
	v_mov_b64_e32 v[44:45], v[40:41]
	s_nop 3
	s_nop 1
	v_mfma_f32_16x16x32_bf16 v[4:7], v[36:39], v[44:47], v[4:7]
	v_mov_b64_e32 v[46:47], v[42:43]
	ds_read_b128 v[36:39], v0 offset:39296
	v_mov_b64_e32 v[44:45], v[40:41]
	s_waitcnt lgkmcnt(0)
	s_nop 3
	s_nop 0
	v_mfma_f32_16x16x32_bf16 v[12:15], v[36:39], v[44:47], v[12:15]
	v_mov_b64_e32 v[46:47], v[42:43]
	ds_read_b128 v[36:39], v0 offset:43648
	v_mov_b64_e32 v[44:45], v[40:41]
	s_waitcnt lgkmcnt(0)
	s_nop 3
	s_nop 0
	v_mfma_f32_16x16x32_bf16 v[16:19], v[36:39], v[44:47], v[16:19]
	v_mov_b64_e32 v[46:47], v[42:43]
	ds_read_b128 v[36:39], v0 offset:48000
	v_mov_b64_e32 v[44:45], v[40:41]
	s_waitcnt lgkmcnt(0)
; #define LAS __attribute__((address_space(3)))
; DI f32x4 mfma16(bf16x8 a, bf16x8 b, f32x4 c) { asm volatile("s_nop 3" : "+v"(a), "+v"(b)); return __builtin_amdgcn_mfma_f32_16x16x32_bf16(a, b, c, 0, 0, 0); }
; DI void ssd_local_unit(Frame& F, int l, int ch, int g) {
;     ...
; #pragma unroll
;     for (int ks = 0; ks < 4; ++ks) { const bf16x8 a = *(const LAS bf16x8*)(XWT + (16 * w + r) * LP + 32 * ks + 8 * q);
; #pragma unroll
;         for (int nt = 0; nt < 8; ++nt) { const bf16x8 b = *(const LAS bf16x8*)(BT + (16 * nt + r) * LP + 32 * ks + 8 * q); acc[nt] = mfma16(a, b, acc[nt]); } }
;     float* sst = (float*)(F.ws + WS_SST);
; #pragma unroll
;     for (int jj = 0; jj < 4; ++jj) { const int row = 16 * w + 4 * q + jj, head = 2 * g + (row >> 6), p = row & 63;
;         float* o = sst + ((size_t)(ch * 4 + head) * 64 + p) * 128 + r;
; #pragma unroll
;         for (int nt = 0; nt < 8; ++nt) o[16 * nt] = acc[nt][jj]; }
;     if (F.tid < 2) ((float*)(F.ws + WS_SMALL))[ch * 4 + 2 * g + F.tid] = __expf(AC[F.tid * 128 + 127]);
	s_nop 3
	s_nop 0
	v_mfma_f32_16x16x32_bf16 v[20:23], v[36:39], v[44:47], v[20:23]
	v_mov_b64_e32 v[46:47], v[42:43]
	ds_read_b128 v[36:39], v0 offset:52352
	v_mov_b64_e32 v[44:45], v[40:41]
	s_waitcnt lgkmcnt(0)
	s_nop 3
	s_nop 0
	v_mfma_f32_16x16x32_bf16 v[24:27], v[36:39], v[44:47], v[24:27]
	v_mov_b64_e32 v[46:47], v[42:43]
	ds_read_b128 v[36:39], v0 offset:56704
	v_mov_b64_e32 v[44:45], v[40:41]
	s_waitcnt lgkmcnt(0)
	s_nop 3
	s_nop 0
	v_mfma_f32_16x16x32_bf16 v[28:31], v[36:39], v[44:47], v[28:31]
	v_mov_b64_e32 v[46:47], v[42:43]
	ds_read_b128 v[36:39], v0 offset:61056
	v_mov_b64_e32 v[44:45], v[40:41]
	s_waitcnt lgkmcnt(0)
	s_nop 3
	s_nop 0
	v_mfma_f32_16x16x32_bf16 v[32:35], v[36:39], v[44:47], v[32:35]
	ds_read_b128 v[36:39], v0 offset:65408
	s_waitcnt lgkmcnt(0)
	s_nop 3
	s_nop 0
	v_mfma_f32_16x16x32_bf16 v[36:39], v[36:39], v[40:43], v[8:11]
	s_nop 2
	ds_read_b128 v[8:11], v0 offset:35008
	ds_read_b128 v[40:43], v48 offset:192
	s_waitcnt lgkmcnt(0)
	v_mov_b64_e32 v[46:47], v[42:43]
	v_mov_b64_e32 v[44:45], v[40:41]
	s_nop 3
	s_nop 1
	v_mfma_f32_16x16x32_bf16 v[4:7], v[8:11], v[44:47], v[4:7]
	v_mov_b64_e32 v[46:47], v[42:43]
	ds_read_b128 v[8:11], v0 offset:39360
	v_mov_b64_e32 v[44:45], v[40:41]
	s_waitcnt lgkmcnt(0)
	s_nop 3
	s_nop 0
	v_mfma_f32_16x16x32_bf16 v[8:11], v[8:11], v[44:47], v[12:15]
	v_mov_b64_e32 v[46:47], v[42:43]
	v_mov_b64_e32 v[44:45], v[40:41]
	s_nop 0
	ds_read_b128 v[12:15], v0 offset:43712
	s_waitcnt lgkmcnt(0)
	s_nop 3
	s_nop 0
	v_mfma_f32_16x16x32_bf16 v[12:15], v[12:15], v[44:47], v[16:19]
	v_mov_b64_e32 v[46:47], v[42:43]
	v_mov_b64_e32 v[44:45], v[40:41]
	s_nop 0
	ds_read_b128 v[16:19], v0 offset:48064
	s_waitcnt lgkmcnt(0)
	s_nop 3
	s_nop 0
	v_mfma_f32_16x16x32_bf16 v[16:19], v[16:19], v[44:47], v[20:23]
	v_mov_b64_e32 v[46:47], v[42:43]
	v_mov_b64_e32 v[44:45], v[40:41]
	s_nop 0
	ds_read_b128 v[20:23], v0 offset:52416
	s_waitcnt lgkmcnt(0)
	s_nop 3
	s_nop 0
	v_mfma_f32_16x16x32_bf16 v[20:23], v[20:23], v[44:47], v[24:27]
	v_mov_b64_e32 v[46:47], v[42:43]
	v_mov_b64_e32 v[44:45], v[40:41]
	s_nop 0
	ds_read_b128 v[24:27], v0 offset:56768
	s_waitcnt lgkmcnt(0)
	s_nop 3
	s_nop 0
	v_mfma_f32_16x16x32_bf16 v[24:27], v[24:27], v[44:47], v[28:31]
	v_mov_b64_e32 v[46:47], v[42:43]
	v_mov_b64_e32 v[44:45], v[40:41]
	s_nop 0
	ds_read_b128 v[28:31], v0 offset:61120
	s_waitcnt lgkmcnt(0)
	s_nop 3
	s_nop 0
	v_mfma_f32_16x16x32_bf16 v[28:31], v[28:31], v[44:47], v[32:35]
	s_nop 2
	ds_read_b128 v[32:35], v0 offset:65472
	s_waitcnt lgkmcnt(0)
	s_nop 3
	v_lshlrev_b32_e32 v0, 7, v133
	v_mfma_f32_16x16x32_bf16 v[32:35], v[32:35], v[40:43], v[36:39]
	s_nop 2
	v_lshl_add_u64 v[36:37], s[0:1], 0, v[2:3]
	s_lshl_b32 s0, s37, 13
	v_mov_b32_e32 v2, s0
	s_movk_i32 s0, 0x7800
	v_bitop3_b32 v2, v0, s0, v2 bitop3:0xc8
	v_lshl_add_u64 v[38:39], v[36:37], 0, v[2:3]
	s_mov_b64 s[0:1], 0x1f100000
	v_lshl_add_u64 v[36:37], v[38:39], 0, s[0:1]
	s_mov_b32 s0, 0x1f100000
	v_add_co_u32_e32 v38, vcc, s0, v38
	s_nop 1
	v_addc_co_u32_e32 v39, vcc, 0, v39, vcc
	v_cmp_gt_i32_e32 vcc, 2, v132
	v_and_b32_e32 v40, 15, v133
	v_lshrrev_b32_e32 v41, 4, v133
	v_mul_u32_u24_e32 v40, 0x1fc, v40
	v_mul_u32_u24_e32 v41, 0x7f0, v41
	v_sub_u32_e32 v40, v40, v41
	v_ashrrev_i32_e32 v41, 31, v40
	v_lshl_add_u64 v[36:37], v[36:37], 0, v[40:41]
	s_nop 7
	global_store_dwordx4 v[36:37], v[4:7], off
	global_store_dwordx4 v[36:37], v[8:11], off offset:64
	global_store_dwordx4 v[36:37], v[12:15], off offset:128
	global_store_dwordx4 v[36:37], v[16:19], off offset:192
	global_store_dwordx4 v[36:37], v[20:23], off offset:256
	global_store_dwordx4 v[36:37], v[24:27], off offset:320
	global_store_dwordx4 v[36:37], v[28:31], off offset:384
	global_store_dwordx4 v[36:37], v[32:35], off offset:448
	s_and_saveexec_b64 s[0:1], vcc
	s_cbranch_execz .LBB0_840
	v_lshl_add_u32 v0, v132, 9, s36
	ds_read_b32 v0, v0 offset:508
	v_add_u32_e32 v4, s2, v132
	v_ashrrev_i32_e32 v5, 31, v4
	v_lshl_add_u64 v[4:5], v[4:5], 2, s[20:21]
	v_add_co_u32_e32 v4, vcc, 0x300000, v4
	s_waitcnt lgkmcnt(0)
	v_mul_f32_e32 v0, 0x3fb8aa3b, v0
	v_exp_f32_e32 v0, v0
	v_addc_co_u32_e32 v5, vcc, 0, v5, vcc
	global_store_dword v[4:5], v0, off
